# edge-trimmed GEMM K-loops plus A-fragment LDS reads issued under the previous phase MFMAs (lighter load sections)
# speedup vs baseline: 1.0075x; 1.0075x over previous
.LBB0_266:
	s_add_u32 s14, s14, 0x80
	s_addc_u32 s15, s15, 0
	s_add_u32 s38, s16, 0x100
	v_mov_b32_e32 v8, 0
	s_addc_u32 s39, s17, 0
	s_mov_b32 s40, -2
	v_mov_b32_e32 v9, v8
	v_mov_b32_e32 v10, v8
	v_mov_b32_e32 v11, v8
	v_mov_b32_e32 v16, v8
	v_mov_b32_e32 v17, v8
	v_mov_b32_e32 v18, v8
	v_mov_b32_e32 v19, v8
	v_mov_b32_e32 v28, v8
	v_mov_b32_e32 v29, v8
	v_mov_b32_e32 v30, v8
	v_mov_b32_e32 v31, v8
	v_mov_b32_e32 v40, v8
	v_mov_b32_e32 v41, v8
	v_mov_b32_e32 v42, v8
	v_mov_b32_e32 v43, v8
	v_mov_b32_e32 v0, v8
	v_mov_b32_e32 v1, v8
	v_mov_b32_e32 v2, v8
	v_mov_b32_e32 v3, v8
	v_mov_b32_e32 v4, v8
	v_mov_b32_e32 v5, v8
	v_mov_b32_e32 v6, v8
	v_mov_b32_e32 v7, v8
	v_mov_b32_e32 v12, v8
	v_mov_b32_e32 v13, v8
	v_mov_b32_e32 v14, v8
	v_mov_b32_e32 v15, v8
	v_mov_b32_e32 v20, v8
	v_mov_b32_e32 v21, v8
	v_mov_b32_e32 v22, v8
	v_mov_b32_e32 v23, v8
	v_mov_b32_e32 v36, v8
	v_mov_b32_e32 v37, v8
	v_mov_b32_e32 v38, v8
	v_mov_b32_e32 v39, v8
	v_mov_b32_e32 v44, v8
	v_mov_b32_e32 v45, v8
	v_mov_b32_e32 v46, v8
	v_mov_b32_e32 v47, v8
	v_mov_b32_e32 v56, v8
	v_mov_b32_e32 v57, v8
	v_mov_b32_e32 v58, v8
	v_mov_b32_e32 v59, v8
	v_mov_b32_e32 v60, v8
	v_mov_b32_e32 v61, v8
	v_mov_b32_e32 v62, v8
	v_mov_b32_e32 v63, v8
	v_mov_b32_e32 v64, v8
	v_mov_b32_e32 v65, v8
	v_mov_b32_e32 v66, v8
	v_mov_b32_e32 v67, v8
	v_mov_b32_e32 v68, v8
	v_mov_b32_e32 v69, v8
	v_mov_b32_e32 v70, v8
	v_mov_b32_e32 v71, v8
	v_mov_b32_e32 v72, v8
	v_mov_b32_e32 v73, v8
	v_mov_b32_e32 v74, v8
	v_mov_b32_e32 v75, v8
	v_mov_b32_e32 v80, v8
	v_mov_b32_e32 v81, v8
	v_mov_b32_e32 v82, v8
	v_mov_b32_e32 v83, v8
	v_mov_b32_e32 v88, v8
	v_mov_b32_e32 v89, v8
	v_mov_b32_e32 v90, v8
	v_mov_b32_e32 v91, v8
	v_mov_b32_e32 v96, v8
	v_mov_b32_e32 v97, v8
	v_mov_b32_e32 v98, v8
	v_mov_b32_e32 v99, v8
	v_mov_b32_e32 v104, v8
	v_mov_b32_e32 v105, v8
	v_mov_b32_e32 v106, v8
	v_mov_b32_e32 v107, v8
	v_mov_b32_e32 v112, v8
	v_mov_b32_e32 v113, v8
	v_mov_b32_e32 v114, v8
	v_mov_b32_e32 v115, v8
	v_mov_b32_e32 v76, v8
	v_mov_b32_e32 v77, v8
	v_mov_b32_e32 v78, v8
	v_mov_b32_e32 v79, v8
	v_mov_b32_e32 v84, v8
	v_mov_b32_e32 v85, v8
	v_mov_b32_e32 v86, v8
	v_mov_b32_e32 v87, v8
	v_mov_b32_e32 v92, v8
	v_mov_b32_e32 v93, v8
	v_mov_b32_e32 v94, v8
	v_mov_b32_e32 v95, v8
	v_mov_b32_e32 v100, v8
	v_mov_b32_e32 v101, v8
	v_mov_b32_e32 v102, v8
	v_mov_b32_e32 v103, v8
	v_mov_b32_e32 v108, v8
	v_mov_b32_e32 v109, v8
	v_mov_b32_e32 v110, v8
	v_mov_b32_e32 v111, v8
	v_mov_b32_e32 v116, v8
	v_mov_b32_e32 v117, v8
	v_mov_b32_e32 v118, v8
	v_mov_b32_e32 v119, v8
	v_mov_b32_e32 v120, v8
	v_mov_b32_e32 v121, v8
	v_mov_b32_e32 v122, v8
	v_mov_b32_e32 v123, v8
	v_mov_b32_e32 v124, v8
	v_mov_b32_e32 v125, v8
	v_mov_b32_e32 v126, v8
	v_mov_b32_e32 v127, v8
	v_mov_b32_e32 v52, v8
	v_mov_b32_e32 v53, v8
	v_mov_b32_e32 v54, v8
	v_mov_b32_e32 v55, v8
	v_mov_b32_e32 v48, v8
	v_mov_b32_e32 v49, v8
	v_mov_b32_e32 v50, v8
	v_mov_b32_e32 v51, v8
	v_mov_b32_e32 v32, v8
	v_mov_b32_e32 v33, v8
	v_mov_b32_e32 v34, v8
	v_mov_b32_e32 v35, v8
	v_mov_b32_e32 v24, v8
	v_mov_b32_e32 v25, v8
	v_mov_b32_e32 v26, v8
	v_mov_b32_e32 v27, v8
	ds_read_b128 v[172:175], v148
	ds_read_b128 v[176:179], v148 offset:1024
	ds_read_b128 v[180:183], v148 offset:2048
	ds_read_b128 v[208:211], v148 offset:3072
	ds_read_b128 v[212:215], v148 offset:4096
	ds_read_b128 v[216:219], v148 offset:5120
	ds_read_b128 v[220:223], v148 offset:6144
	ds_read_b128 v[224:227], v148 offset:7168
.LBB0_267:
	s_add_u32 s16, s14, 0x80
	s_addc_u32 s17, s15, 0
	s_add_i32 s41, 0, 0x10000
	v_add_u32_e32 v144, s41, v147
	ds_read_b128 v[150:153], v144
	ds_read_b128 v[154:157], v144 offset:1024
	ds_read_b128 v[158:161], v144 offset:2048
	ds_read_b128 v[162:165], v144 offset:3072
	s_cmp_eq_u32 s40, 28
	s_cselect_b32 s19, s11, s17
	s_cselect_b32 s18, s10, s16
	s_cselect_b32 s17, s13, s39
	s_cselect_b32 s16, s12, s38
	v_lshl_add_u64 v[144:145], s[14:15], 0, v[142:143]
	s_add_i32 m0, s27, 0xc000
	s_nop 0
	global_load_lds_dwordx4 v[144:145], off
	v_lshl_add_u64 v[144:145], s[14:15], 0, v[140:141]
	s_add_i32 m0, s27, 0xe000
	s_nop 0
	global_load_lds_dwordx4 v[144:145], off
	s_waitcnt lgkmcnt(0)
	s_setprio 1
	s_barrier
	s_waitcnt lgkmcnt(0)
	v_mfma_f32_16x16x32_bf16 v[124:127], v[150:153], v[172:175], v[124:127]
	v_mfma_f32_16x16x32_bf16 v[120:123], v[158:161], v[172:175], v[120:123]
	v_mfma_f32_16x16x32_bf16 v[116:119], v[150:153], v[180:183], v[116:119]
	v_mfma_f32_16x16x32_bf16 v[108:111], v[158:161], v[180:183], v[108:111]
	v_mfma_f32_16x16x32_bf16 v[100:103], v[150:153], v[212:215], v[100:103]
	v_mfma_f32_16x16x32_bf16 v[92:95], v[158:161], v[212:215], v[92:95]
	v_mfma_f32_16x16x32_bf16 v[84:87], v[150:153], v[220:223], v[84:87]
	v_mfma_f32_16x16x32_bf16 v[76:79], v[158:161], v[220:223], v[76:79]
	v_mfma_f32_16x16x32_bf16 v[124:127], v[154:157], v[176:179], v[124:127]
	v_mfma_f32_16x16x32_bf16 v[120:123], v[162:165], v[176:179], v[120:123]
	v_mfma_f32_16x16x32_bf16 v[116:119], v[154:157], v[208:211], v[116:119]
	v_mfma_f32_16x16x32_bf16 v[108:111], v[162:165], v[208:211], v[108:111]
	v_mfma_f32_16x16x32_bf16 v[100:103], v[154:157], v[216:219], v[100:103]
	v_mfma_f32_16x16x32_bf16 v[92:95], v[162:165], v[216:219], v[92:95]
	v_mfma_f32_16x16x32_bf16 v[84:87], v[154:157], v[224:227], v[84:87]
	v_mfma_f32_16x16x32_bf16 v[76:79], v[162:165], v[224:227], v[76:79]
	s_barrier
	s_setprio 0
	s_add_i32 s44, 0, 0x14000
	v_add_u32_e32 v144, s44, v147
	s_add_i32 s41, s41, s25
	ds_read_b128 v[228:231], v144
	ds_read_b128 v[232:235], v144 offset:1024
	ds_read_b128 v[236:239], v144 offset:2048
	ds_read_b128 v[240:243], v144 offset:3072
	v_lshl_add_u64 v[144:145], s[16:17], 0, v[138:139]
	s_mov_b32 m0, s41
	v_lshl_add_u64 v[166:167], s[16:17], 0, v[132:133]
	global_load_lds_dwordx4 v[144:145], off
	s_add_i32 m0, s41, 0x2000
	s_nop 0
	global_load_lds_dwordx4 v[166:167], off
	s_setprio 1
	s_barrier
	s_waitcnt lgkmcnt(0)
	v_mfma_f32_16x16x32_bf16 v[112:115], v[228:231], v[172:175], v[112:115]
	v_mfma_f32_16x16x32_bf16 v[104:107], v[236:239], v[172:175], v[104:107]
	ds_read_b128 v[172:175], v148 offset:16384
	v_mfma_f32_16x16x32_bf16 v[96:99], v[228:231], v[180:183], v[96:99]
	v_mfma_f32_16x16x32_bf16 v[88:91], v[236:239], v[180:183], v[88:91]
	ds_read_b128 v[180:183], v148 offset:18432
	v_mfma_f32_16x16x32_bf16 v[80:83], v[228:231], v[212:215], v[80:83]
	v_mfma_f32_16x16x32_bf16 v[72:75], v[236:239], v[212:215], v[72:75]
	ds_read_b128 v[212:215], v148 offset:20480
	v_mfma_f32_16x16x32_bf16 v[68:71], v[228:231], v[220:223], v[68:71]
	v_mfma_f32_16x16x32_bf16 v[64:67], v[236:239], v[220:223], v[64:67]
	ds_read_b128 v[220:223], v148 offset:22528
	v_mfma_f32_16x16x32_bf16 v[112:115], v[232:235], v[176:179], v[112:115]
	v_mfma_f32_16x16x32_bf16 v[104:107], v[240:243], v[176:179], v[104:107]
	ds_read_b128 v[176:179], v148 offset:17408
	v_mfma_f32_16x16x32_bf16 v[96:99], v[232:235], v[208:211], v[96:99]
	v_mfma_f32_16x16x32_bf16 v[88:91], v[240:243], v[208:211], v[88:91]
	ds_read_b128 v[208:211], v148 offset:19456
	v_mfma_f32_16x16x32_bf16 v[80:83], v[232:235], v[216:219], v[80:83]
	v_mfma_f32_16x16x32_bf16 v[72:75], v[240:243], v[216:219], v[72:75]
	ds_read_b128 v[216:219], v148 offset:21504
	v_mfma_f32_16x16x32_bf16 v[68:71], v[232:235], v[224:227], v[68:71]
	v_mfma_f32_16x16x32_bf16 v[64:67], v[240:243], v[224:227], v[64:67]
	ds_read_b128 v[224:227], v148 offset:23552
	s_barrier
	s_setprio 0
	s_mov_b32 m0, s27
	v_lshl_add_u64 v[184:185], s[18:19], 0, v[134:135]
	global_load_lds_dwordx4 v[184:185], off
	v_lshl_add_u64 v[244:245], s[18:19], 0, v[128:129]
	s_mov_b32 m0, s28
	s_nop 0
	global_load_lds_dwordx4 v[244:245], off
	s_waitcnt vmcnt(8)
	s_setprio 1
	s_barrier
	s_waitcnt lgkmcnt(0)
	v_mfma_f32_16x16x32_bf16 v[60:63], v[150:153], v[172:175], v[60:63]
	v_mfma_f32_16x16x32_bf16 v[56:59], v[158:161], v[172:175], v[56:59]
	v_mfma_f32_16x16x32_bf16 v[44:47], v[150:153], v[180:183], v[44:47]
	v_mfma_f32_16x16x32_bf16 v[36:39], v[158:161], v[180:183], v[36:39]
	v_mfma_f32_16x16x32_bf16 v[20:23], v[150:153], v[212:215], v[20:23]
	v_mfma_f32_16x16x32_bf16 v[12:15], v[158:161], v[212:215], v[12:15]
	v_mfma_f32_16x16x32_bf16 v[4:7], v[150:153], v[220:223], v[4:7]
	v_mfma_f32_16x16x32_bf16 v[0:3], v[158:161], v[220:223], v[0:3]
	v_mfma_f32_16x16x32_bf16 v[60:63], v[154:157], v[176:179], v[60:63]
	v_mfma_f32_16x16x32_bf16 v[56:59], v[162:165], v[176:179], v[56:59]
	v_mfma_f32_16x16x32_bf16 v[44:47], v[154:157], v[208:211], v[44:47]
	v_mfma_f32_16x16x32_bf16 v[36:39], v[162:165], v[208:211], v[36:39]
	v_mfma_f32_16x16x32_bf16 v[20:23], v[154:157], v[216:219], v[20:23]
	v_mfma_f32_16x16x32_bf16 v[12:15], v[162:165], v[216:219], v[12:15]
	v_mfma_f32_16x16x32_bf16 v[4:7], v[154:157], v[224:227], v[4:7]
	v_mfma_f32_16x16x32_bf16 v[0:3], v[162:165], v[224:227], v[0:3]
	s_barrier
	s_setprio 0
	s_add_u32 s42, s16, 0x80000
	s_addc_u32 s43, s17, 0
	s_add_i32 s41, s44, s25
	v_lshl_add_u64 v[150:151], s[42:43], 0, v[138:139]
	s_mov_b32 m0, s41
	s_nop 0
	global_load_lds_dwordx4 v[150:151], off
	v_lshl_add_u64 v[150:151], s[42:43], 0, v[132:133]
	s_add_i32 m0, s41, 0x2000
	s_nop 0
	global_load_lds_dwordx4 v[150:151], off
	s_waitcnt vmcnt(6)
	s_setprio 1
	s_barrier
	v_mfma_f32_16x16x32_bf16 v[40:43], v[228:231], v[172:175], v[40:43]
	v_mfma_f32_16x16x32_bf16 v[28:31], v[236:239], v[172:175], v[28:31]
	ds_read_b128 v[172:175], v148 offset:32768
	v_mfma_f32_16x16x32_bf16 v[16:19], v[228:231], v[180:183], v[16:19]
	v_mfma_f32_16x16x32_bf16 v[8:11], v[236:239], v[180:183], v[8:11]
	ds_read_b128 v[180:183], v148 offset:34816
	v_mfma_f32_16x16x32_bf16 v[52:55], v[228:231], v[212:215], v[52:55]
	v_mfma_f32_16x16x32_bf16 v[48:51], v[236:239], v[212:215], v[48:51]
	ds_read_b128 v[212:215], v148 offset:36864
	v_mfma_f32_16x16x32_bf16 v[32:35], v[228:231], v[220:223], v[32:35]
	v_mfma_f32_16x16x32_bf16 v[24:27], v[236:239], v[220:223], v[24:27]
	ds_read_b128 v[220:223], v148 offset:38912
	v_mfma_f32_16x16x32_bf16 v[40:43], v[232:235], v[176:179], v[40:43]
	v_mfma_f32_16x16x32_bf16 v[28:31], v[240:243], v[176:179], v[28:31]
	ds_read_b128 v[176:179], v148 offset:33792
	v_mfma_f32_16x16x32_bf16 v[16:19], v[232:235], v[208:211], v[16:19]
	v_mfma_f32_16x16x32_bf16 v[8:11], v[240:243], v[208:211], v[8:11]
	ds_read_b128 v[208:211], v148 offset:35840
	v_mfma_f32_16x16x32_bf16 v[52:55], v[232:235], v[216:219], v[52:55]
	v_mfma_f32_16x16x32_bf16 v[48:51], v[240:243], v[216:219], v[48:51]
	ds_read_b128 v[216:219], v148 offset:37888
	v_mfma_f32_16x16x32_bf16 v[32:35], v[232:235], v[224:227], v[32:35]
	v_mfma_f32_16x16x32_bf16 v[24:27], v[240:243], v[224:227], v[24:27]
	ds_read_b128 v[224:227], v148 offset:39936
	s_barrier
	s_setprio 0
	s_add_i32 s41, 0, 0x18000
	v_add_u32_e32 v149, s41, v147
	ds_read_b128 v[150:153], v149
	ds_read_b128 v[154:157], v149 offset:1024
	ds_read_b128 v[158:161], v149 offset:2048
	ds_read_b128 v[162:165], v149 offset:3072
	s_mov_b32 m0, s29
	v_lshl_add_u64 v[228:229], s[18:19], 0, v[136:137]
	global_load_lds_dwordx4 v[228:229], off
	v_lshl_add_u64 v[228:229], s[18:19], 0, v[130:131]
	s_mov_b32 m0, s30
	s_nop 0
	global_load_lds_dwordx4 v[228:229], off
	s_waitcnt lgkmcnt(0)
	s_setprio 1
	s_barrier
	s_waitcnt lgkmcnt(0)
	v_mfma_f32_16x16x32_bf16 v[124:127], v[150:153], v[172:175], v[124:127]
	v_mfma_f32_16x16x32_bf16 v[120:123], v[158:161], v[172:175], v[120:123]
	v_mfma_f32_16x16x32_bf16 v[116:119], v[150:153], v[180:183], v[116:119]
	v_mfma_f32_16x16x32_bf16 v[108:111], v[158:161], v[180:183], v[108:111]
	v_mfma_f32_16x16x32_bf16 v[100:103], v[150:153], v[212:215], v[100:103]
	v_mfma_f32_16x16x32_bf16 v[92:95], v[158:161], v[212:215], v[92:95]
	v_mfma_f32_16x16x32_bf16 v[84:87], v[150:153], v[220:223], v[84:87]
	v_mfma_f32_16x16x32_bf16 v[76:79], v[158:161], v[220:223], v[76:79]
	v_mfma_f32_16x16x32_bf16 v[124:127], v[154:157], v[176:179], v[124:127]
	v_mfma_f32_16x16x32_bf16 v[120:123], v[162:165], v[176:179], v[120:123]
	v_mfma_f32_16x16x32_bf16 v[116:119], v[154:157], v[208:211], v[116:119]
	v_mfma_f32_16x16x32_bf16 v[108:111], v[162:165], v[208:211], v[108:111]
	v_mfma_f32_16x16x32_bf16 v[100:103], v[154:157], v[216:219], v[100:103]
	v_mfma_f32_16x16x32_bf16 v[92:95], v[162:165], v[216:219], v[92:95]
	v_mfma_f32_16x16x32_bf16 v[84:87], v[154:157], v[224:227], v[84:87]
	v_mfma_f32_16x16x32_bf16 v[76:79], v[162:165], v[224:227], v[76:79]
	s_barrier
	s_setprio 0
	s_add_i32 s18, 0, 0x1c000
	s_add_i32 s19, s41, s25
	v_add_u32_e32 v149, s18, v147
	v_lshl_add_u64 v[144:145], v[144:145], 0, s[94:95]
	s_mov_b32 m0, s19
	ds_read_b128 v[228:231], v149
	ds_read_b128 v[232:235], v149 offset:1024
	ds_read_b128 v[236:239], v149 offset:2048
	ds_read_b128 v[240:243], v149 offset:3072
	global_load_lds_dwordx4 v[144:145], off
	v_lshl_add_u64 v[144:145], v[166:167], 0, s[94:95]
	s_add_i32 m0, s19, 0x2000
	s_nop 0
	global_load_lds_dwordx4 v[144:145], off
	s_setprio 1
	s_barrier
	s_waitcnt lgkmcnt(0)
	v_mfma_f32_16x16x32_bf16 v[112:115], v[228:231], v[172:175], v[112:115]
	v_mfma_f32_16x16x32_bf16 v[104:107], v[236:239], v[172:175], v[104:107]
	ds_read_b128 v[172:175], v148 offset:49152
	v_mfma_f32_16x16x32_bf16 v[96:99], v[228:231], v[180:183], v[96:99]
	v_mfma_f32_16x16x32_bf16 v[88:91], v[236:239], v[180:183], v[88:91]
	ds_read_b128 v[180:183], v148 offset:51200
	v_mfma_f32_16x16x32_bf16 v[80:83], v[228:231], v[212:215], v[80:83]
	v_mfma_f32_16x16x32_bf16 v[72:75], v[236:239], v[212:215], v[72:75]
	ds_read_b128 v[212:215], v148 offset:53248
	v_mfma_f32_16x16x32_bf16 v[68:71], v[228:231], v[220:223], v[68:71]
	v_mfma_f32_16x16x32_bf16 v[64:67], v[236:239], v[220:223], v[64:67]
	ds_read_b128 v[220:223], v148 offset:55296
	v_mfma_f32_16x16x32_bf16 v[112:115], v[232:235], v[176:179], v[112:115]
	v_mfma_f32_16x16x32_bf16 v[104:107], v[240:243], v[176:179], v[104:107]
	ds_read_b128 v[176:179], v148 offset:50176
	v_mfma_f32_16x16x32_bf16 v[96:99], v[232:235], v[208:211], v[96:99]
	v_mfma_f32_16x16x32_bf16 v[88:91], v[240:243], v[208:211], v[88:91]
	ds_read_b128 v[208:211], v148 offset:52224
	v_mfma_f32_16x16x32_bf16 v[80:83], v[232:235], v[216:219], v[80:83]
	v_mfma_f32_16x16x32_bf16 v[72:75], v[240:243], v[216:219], v[72:75]
	ds_read_b128 v[216:219], v148 offset:54272
	v_mfma_f32_16x16x32_bf16 v[68:71], v[232:235], v[224:227], v[68:71]
	v_mfma_f32_16x16x32_bf16 v[64:67], v[240:243], v[224:227], v[64:67]
	ds_read_b128 v[224:227], v148 offset:56320
	s_barrier
	s_setprio 0
	s_mov_b32 m0, s31
	v_lshl_add_u64 v[144:145], v[184:185], 0, s[94:95]
	global_load_lds_dwordx4 v[144:145], off
	v_lshl_add_u64 v[144:145], v[244:245], 0, s[94:95]
	s_mov_b32 m0, s34
	s_nop 0
	global_load_lds_dwordx4 v[144:145], off
	s_waitcnt vmcnt(8)
	s_setprio 1
	s_barrier
	s_waitcnt lgkmcnt(0)
	v_mfma_f32_16x16x32_bf16 v[60:63], v[150:153], v[172:175], v[60:63]
	v_mfma_f32_16x16x32_bf16 v[56:59], v[158:161], v[172:175], v[56:59]
	v_mfma_f32_16x16x32_bf16 v[44:47], v[150:153], v[180:183], v[44:47]
	v_mfma_f32_16x16x32_bf16 v[36:39], v[158:161], v[180:183], v[36:39]
	v_mfma_f32_16x16x32_bf16 v[20:23], v[150:153], v[212:215], v[20:23]
	v_mfma_f32_16x16x32_bf16 v[12:15], v[158:161], v[212:215], v[12:15]
	v_mfma_f32_16x16x32_bf16 v[4:7], v[150:153], v[220:223], v[4:7]
	v_mfma_f32_16x16x32_bf16 v[0:3], v[158:161], v[220:223], v[0:3]
	v_mfma_f32_16x16x32_bf16 v[60:63], v[154:157], v[176:179], v[60:63]
	v_mfma_f32_16x16x32_bf16 v[56:59], v[162:165], v[176:179], v[56:59]
	v_mfma_f32_16x16x32_bf16 v[44:47], v[154:157], v[208:211], v[44:47]
	v_mfma_f32_16x16x32_bf16 v[36:39], v[162:165], v[208:211], v[36:39]
	v_mfma_f32_16x16x32_bf16 v[20:23], v[154:157], v[216:219], v[20:23]
	v_mfma_f32_16x16x32_bf16 v[12:15], v[162:165], v[216:219], v[12:15]
	v_mfma_f32_16x16x32_bf16 v[4:7], v[154:157], v[224:227], v[4:7]
	v_mfma_f32_16x16x32_bf16 v[0:3], v[162:165], v[224:227], v[0:3]
	s_barrier
	s_setprio 0
	s_add_u32 s16, s16, 0x80080
	s_addc_u32 s17, s17, 0
	s_add_i32 s18, s18, s25
	v_lshl_add_u64 v[144:145], s[16:17], 0, v[138:139]
	s_mov_b32 m0, s18
	s_nop 0
	global_load_lds_dwordx4 v[144:145], off
	v_lshl_add_u64 v[144:145], s[16:17], 0, v[132:133]
	s_add_i32 m0, s18, 0x2000
	s_nop 0
	global_load_lds_dwordx4 v[144:145], off
	s_waitcnt vmcnt(6)
	s_setprio 1
	s_barrier
	v_mfma_f32_16x16x32_bf16 v[40:43], v[228:231], v[172:175], v[40:43]
	v_mfma_f32_16x16x32_bf16 v[28:31], v[236:239], v[172:175], v[28:31]
	ds_read_b128 v[172:175], v148
	v_mfma_f32_16x16x32_bf16 v[16:19], v[228:231], v[180:183], v[16:19]
	v_mfma_f32_16x16x32_bf16 v[8:11], v[236:239], v[180:183], v[8:11]
	ds_read_b128 v[180:183], v148 offset:2048
	v_mfma_f32_16x16x32_bf16 v[52:55], v[228:231], v[212:215], v[52:55]
	v_mfma_f32_16x16x32_bf16 v[48:51], v[236:239], v[212:215], v[48:51]
	ds_read_b128 v[212:215], v148 offset:4096
	v_mfma_f32_16x16x32_bf16 v[32:35], v[228:231], v[220:223], v[32:35]
	v_mfma_f32_16x16x32_bf16 v[24:27], v[236:239], v[220:223], v[24:27]
	ds_read_b128 v[220:223], v148 offset:6144
	v_mfma_f32_16x16x32_bf16 v[40:43], v[232:235], v[176:179], v[40:43]
	v_mfma_f32_16x16x32_bf16 v[28:31], v[240:243], v[176:179], v[28:31]
	ds_read_b128 v[176:179], v148 offset:1024
	v_mfma_f32_16x16x32_bf16 v[16:19], v[232:235], v[208:211], v[16:19]
	v_mfma_f32_16x16x32_bf16 v[8:11], v[240:243], v[208:211], v[8:11]
	ds_read_b128 v[208:211], v148 offset:3072
	v_mfma_f32_16x16x32_bf16 v[52:55], v[232:235], v[216:219], v[52:55]
	v_mfma_f32_16x16x32_bf16 v[48:51], v[240:243], v[216:219], v[48:51]
	ds_read_b128 v[216:219], v148 offset:5120
	v_mfma_f32_16x16x32_bf16 v[32:35], v[232:235], v[224:227], v[32:35]
	v_mfma_f32_16x16x32_bf16 v[24:27], v[240:243], v[224:227], v[24:27]
	ds_read_b128 v[224:227], v148 offset:7168
	s_barrier
	s_setprio 0
	s_add_i32 s40, s40, 2
	s_add_u32 s14, s14, 0x100
	s_addc_u32 s15, s15, 0
	s_add_u32 s38, s38, 0x100
	s_addc_u32 s39, s39, 0
	s_cmp_gt_u32 s40, 29
	s_cbranch_scc0 .LBB0_267
	s_waitcnt lgkmcnt(0)
	s_and_b64 vcc, exec, s[6:7]
	s_cbranch_vccz .LBB0_270
	s_barrier

.LBB0_1001:
	s_add_u32 s4, s4, 0x80
	s_addc_u32 s5, s5, 0
	s_add_u32 s46, s22, 0x100
	s_waitcnt vmcnt(0)
	v_mov_b32_e32 v32, 0
	s_addc_u32 s47, s23, 0
	s_mov_b32 s48, -2
	v_mov_b32_e32 v33, v32
	v_mov_b32_e32 v34, v32
	v_mov_b32_e32 v35, v32
	v_mov_b32_e32 v36, v32
	v_mov_b32_e32 v37, v32
	v_mov_b32_e32 v38, v32
	v_mov_b32_e32 v39, v32
	v_mov_b32_e32 v48, v32
	v_mov_b32_e32 v49, v32
	v_mov_b32_e32 v50, v32
	v_mov_b32_e32 v51, v32
	v_mov_b32_e32 v52, v32
	v_mov_b32_e32 v53, v32
	v_mov_b32_e32 v54, v32
	v_mov_b32_e32 v55, v32
	v_mov_b32_e32 v0, v32
	v_mov_b32_e32 v1, v32
	v_mov_b32_e32 v2, v32
	v_mov_b32_e32 v3, v32
	v_mov_b32_e32 v8, v32
	v_mov_b32_e32 v9, v32
	v_mov_b32_e32 v10, v32
	v_mov_b32_e32 v11, v32
	v_mov_b32_e32 v20, v32
	v_mov_b32_e32 v21, v32
	v_mov_b32_e32 v22, v32
	v_mov_b32_e32 v23, v32
	v_mov_b32_e32 v28, v32
	v_mov_b32_e32 v29, v32
	v_mov_b32_e32 v30, v32
	v_mov_b32_e32 v31, v32
	v_mov_b32_e32 v40, v32
	v_mov_b32_e32 v41, v32
	v_mov_b32_e32 v42, v32
	v_mov_b32_e32 v43, v32
	v_mov_b32_e32 v44, v32
	v_mov_b32_e32 v45, v32
	v_mov_b32_e32 v46, v32
	v_mov_b32_e32 v47, v32
	v_mov_b32_e32 v56, v32
	v_mov_b32_e32 v57, v32
	v_mov_b32_e32 v58, v32
	v_mov_b32_e32 v59, v32
	v_mov_b32_e32 v60, v32
	v_mov_b32_e32 v61, v32
	v_mov_b32_e32 v62, v32
	v_mov_b32_e32 v63, v32
	v_mov_b32_e32 v64, v32
	v_mov_b32_e32 v65, v32
	v_mov_b32_e32 v66, v32
	v_mov_b32_e32 v67, v32
	v_mov_b32_e32 v72, v32
	v_mov_b32_e32 v73, v32
	v_mov_b32_e32 v74, v32
	v_mov_b32_e32 v75, v32
	v_mov_b32_e32 v96, v32
	v_mov_b32_e32 v97, v32
	v_mov_b32_e32 v98, v32
	v_mov_b32_e32 v99, v32
	v_mov_b32_e32 v100, v32
	v_mov_b32_e32 v101, v32
	v_mov_b32_e32 v102, v32
	v_mov_b32_e32 v103, v32
	v_mov_b32_e32 v112, v32
	v_mov_b32_e32 v113, v32
	v_mov_b32_e32 v114, v32
	v_mov_b32_e32 v115, v32
	v_mov_b32_e32 v116, v32
	v_mov_b32_e32 v117, v32
	v_mov_b32_e32 v118, v32
	v_mov_b32_e32 v119, v32
	v_mov_b32_e32 v128, v32
	v_mov_b32_e32 v129, v32
	v_mov_b32_e32 v130, v32
	v_mov_b32_e32 v131, v32
	v_mov_b32_e32 v132, v32
	v_mov_b32_e32 v133, v32
	v_mov_b32_e32 v134, v32
	v_mov_b32_e32 v135, v32
	v_mov_b32_e32 v88, v32
	v_mov_b32_e32 v89, v32
	v_mov_b32_e32 v90, v32
	v_mov_b32_e32 v91, v32
	v_mov_b32_e32 v92, v32
	v_mov_b32_e32 v93, v32
	v_mov_b32_e32 v94, v32
	v_mov_b32_e32 v95, v32
	v_mov_b32_e32 v104, v32
	v_mov_b32_e32 v105, v32
	v_mov_b32_e32 v106, v32
	v_mov_b32_e32 v107, v32
	v_mov_b32_e32 v108, v32
	v_mov_b32_e32 v109, v32
	v_mov_b32_e32 v110, v32
	v_mov_b32_e32 v111, v32
	v_mov_b32_e32 v120, v32
	v_mov_b32_e32 v121, v32
	v_mov_b32_e32 v122, v32
	v_mov_b32_e32 v123, v32
	v_mov_b32_e32 v124, v32
	v_mov_b32_e32 v125, v32
	v_mov_b32_e32 v126, v32
	v_mov_b32_e32 v127, v32
	v_mov_b32_e32 v136, v32
	v_mov_b32_e32 v137, v32
	v_mov_b32_e32 v138, v32
	v_mov_b32_e32 v139, v32
	v_mov_b32_e32 v140, v32
	v_mov_b32_e32 v141, v32
	v_mov_b32_e32 v142, v32
	v_mov_b32_e32 v143, v32
	v_mov_b32_e32 v24, v32
	v_mov_b32_e32 v25, v32
	v_mov_b32_e32 v26, v32
	v_mov_b32_e32 v27, v32
	v_mov_b32_e32 v16, v32
	v_mov_b32_e32 v17, v32
	v_mov_b32_e32 v18, v32
	v_mov_b32_e32 v19, v32
	v_mov_b32_e32 v12, v32
	v_mov_b32_e32 v13, v32
	v_mov_b32_e32 v14, v32
	v_mov_b32_e32 v15, v32
	v_mov_b32_e32 v4, v32
	v_mov_b32_e32 v5, v32
	v_mov_b32_e32 v6, v32
	v_mov_b32_e32 v7, v32
	ds_read_b128 v[144:147], v183
	ds_read_b128 v[148:151], v183 offset:1024
	ds_read_b128 v[172:175], v183 offset:2048
	ds_read_b128 v[176:179], v183 offset:3072
	ds_read_b128 v[208:211], v183 offset:4096
	ds_read_b128 v[212:215], v183 offset:5120
	ds_read_b128 v[216:219], v183 offset:6144
	ds_read_b128 v[220:223], v183 offset:7168
.LBB0_1002:
	s_add_u32 s22, s4, 0x80
	s_addc_u32 s23, s5, 0
	s_add_i32 s49, 0, 0x10000
	v_add_u32_e32 v84, s49, v181
	ds_read_b128 v[68:71], v84
	ds_read_b128 v[76:79], v84 offset:1024
	ds_read_b128 v[80:83], v84 offset:2048
	ds_read_b128 v[84:87], v84 offset:3072
	s_cmp_eq_u32 s48, 28
	s_cselect_b32 s25, s19, s23
	s_cselect_b32 s24, s18, s22
	s_cselect_b32 s23, s21, s47
	s_cselect_b32 s22, s20, s46
	v_lshl_add_u64 v[166:167], s[4:5], 0, v[164:165]
	s_add_i32 m0, s34, 0xc000
	s_nop 0
	global_load_lds_dwordx4 v[166:167], off
	v_lshl_add_u64 v[166:167], s[4:5], 0, v[162:163]
	s_add_i32 m0, s34, 0xe000
	s_nop 0
	global_load_lds_dwordx4 v[166:167], off
	s_waitcnt lgkmcnt(0)
	s_setprio 1
	s_barrier
	s_waitcnt lgkmcnt(0)
	v_mfma_f32_16x16x32_bf16 v[140:143], v[68:71], v[144:147], v[140:143]
	v_mfma_f32_16x16x32_bf16 v[136:139], v[80:83], v[144:147], v[136:139]
	v_mfma_f32_16x16x32_bf16 v[124:127], v[68:71], v[172:175], v[124:127]
	v_mfma_f32_16x16x32_bf16 v[120:123], v[80:83], v[172:175], v[120:123]
	v_mfma_f32_16x16x32_bf16 v[108:111], v[68:71], v[208:211], v[108:111]
	v_mfma_f32_16x16x32_bf16 v[104:107], v[80:83], v[208:211], v[104:107]
	v_mfma_f32_16x16x32_bf16 v[92:95], v[68:71], v[216:219], v[92:95]
	v_mfma_f32_16x16x32_bf16 v[88:91], v[80:83], v[216:219], v[88:91]
	v_mfma_f32_16x16x32_bf16 v[140:143], v[76:79], v[148:151], v[140:143]
	v_mfma_f32_16x16x32_bf16 v[136:139], v[84:87], v[148:151], v[136:139]
	v_mfma_f32_16x16x32_bf16 v[124:127], v[76:79], v[176:179], v[124:127]
	v_mfma_f32_16x16x32_bf16 v[120:123], v[84:87], v[176:179], v[120:123]
	v_mfma_f32_16x16x32_bf16 v[108:111], v[76:79], v[212:215], v[108:111]
	v_mfma_f32_16x16x32_bf16 v[104:107], v[84:87], v[212:215], v[104:107]
	v_mfma_f32_16x16x32_bf16 v[92:95], v[76:79], v[220:223], v[92:95]
	v_mfma_f32_16x16x32_bf16 v[88:91], v[84:87], v[220:223], v[88:91]
	s_barrier
	s_setprio 0
	s_add_i32 s52, 0, 0x14000
	v_add_u32_e32 v166, s52, v181
	s_add_i32 s49, s49, s31
	ds_read_b128 v[224:227], v166
	ds_read_b128 v[228:231], v166 offset:1024
	ds_read_b128 v[232:235], v166 offset:2048
	ds_read_b128 v[236:239], v166 offset:3072
	v_lshl_add_u64 v[166:167], s[22:23], 0, v[168:169]
	s_mov_b32 m0, s49
	v_lshl_add_u64 v[184:185], s[22:23], 0, v[156:157]
	global_load_lds_dwordx4 v[166:167], off
	s_add_i32 m0, s49, 0x2000
	s_nop 0
	global_load_lds_dwordx4 v[184:185], off
	s_setprio 1
	s_barrier
	s_waitcnt lgkmcnt(0)
	v_mfma_f32_16x16x32_bf16 v[132:135], v[224:227], v[144:147], v[132:135]
	v_mfma_f32_16x16x32_bf16 v[128:131], v[232:235], v[144:147], v[128:131]
	ds_read_b128 v[144:147], v183 offset:16384
	v_mfma_f32_16x16x32_bf16 v[116:119], v[224:227], v[172:175], v[116:119]
	v_mfma_f32_16x16x32_bf16 v[112:115], v[232:235], v[172:175], v[112:115]
	ds_read_b128 v[172:175], v183 offset:18432
	v_mfma_f32_16x16x32_bf16 v[100:103], v[224:227], v[208:211], v[100:103]
	v_mfma_f32_16x16x32_bf16 v[96:99], v[232:235], v[208:211], v[96:99]
	ds_read_b128 v[208:211], v183 offset:20480
	v_mfma_f32_16x16x32_bf16 v[72:75], v[224:227], v[216:219], v[72:75]
	v_mfma_f32_16x16x32_bf16 v[64:67], v[232:235], v[216:219], v[64:67]
	ds_read_b128 v[216:219], v183 offset:22528
	v_mfma_f32_16x16x32_bf16 v[132:135], v[228:231], v[148:151], v[132:135]
	v_mfma_f32_16x16x32_bf16 v[128:131], v[236:239], v[148:151], v[128:131]
	ds_read_b128 v[148:151], v183 offset:17408
	v_mfma_f32_16x16x32_bf16 v[116:119], v[228:231], v[176:179], v[116:119]
	v_mfma_f32_16x16x32_bf16 v[112:115], v[236:239], v[176:179], v[112:115]
	ds_read_b128 v[176:179], v183 offset:19456
	v_mfma_f32_16x16x32_bf16 v[100:103], v[228:231], v[212:215], v[100:103]
	v_mfma_f32_16x16x32_bf16 v[96:99], v[236:239], v[212:215], v[96:99]
	ds_read_b128 v[212:215], v183 offset:21504
	v_mfma_f32_16x16x32_bf16 v[72:75], v[228:231], v[220:223], v[72:75]
	v_mfma_f32_16x16x32_bf16 v[64:67], v[236:239], v[220:223], v[64:67]
	ds_read_b128 v[220:223], v183 offset:23552
	s_barrier
	s_setprio 0
	s_mov_b32 m0, s34
	v_lshl_add_u64 v[240:241], s[24:25], 0, v[152:153]
	global_load_lds_dwordx4 v[240:241], off
	v_lshl_add_u64 v[242:243], s[24:25], 0, v[158:159]
	s_mov_b32 m0, s35
	s_nop 0
	global_load_lds_dwordx4 v[242:243], off
	s_waitcnt vmcnt(8)
	s_setprio 1
	s_barrier
	s_waitcnt lgkmcnt(0)
	v_mfma_f32_16x16x32_bf16 v[60:63], v[68:71], v[144:147], v[60:63]
	v_mfma_f32_16x16x32_bf16 v[56:59], v[80:83], v[144:147], v[56:59]
	v_mfma_f32_16x16x32_bf16 v[44:47], v[68:71], v[172:175], v[44:47]
	v_mfma_f32_16x16x32_bf16 v[40:43], v[80:83], v[172:175], v[40:43]
	v_mfma_f32_16x16x32_bf16 v[28:31], v[68:71], v[208:211], v[28:31]
	v_mfma_f32_16x16x32_bf16 v[20:23], v[80:83], v[208:211], v[20:23]
	v_mfma_f32_16x16x32_bf16 v[8:11], v[68:71], v[216:219], v[8:11]
	v_mfma_f32_16x16x32_bf16 v[0:3], v[80:83], v[216:219], v[0:3]
	v_mfma_f32_16x16x32_bf16 v[60:63], v[76:79], v[148:151], v[60:63]
	v_mfma_f32_16x16x32_bf16 v[56:59], v[84:87], v[148:151], v[56:59]
	v_mfma_f32_16x16x32_bf16 v[44:47], v[76:79], v[176:179], v[44:47]
	v_mfma_f32_16x16x32_bf16 v[40:43], v[84:87], v[176:179], v[40:43]
	v_mfma_f32_16x16x32_bf16 v[28:31], v[76:79], v[212:215], v[28:31]
	v_mfma_f32_16x16x32_bf16 v[20:23], v[84:87], v[212:215], v[20:23]
	v_mfma_f32_16x16x32_bf16 v[8:11], v[76:79], v[220:223], v[8:11]
	v_mfma_f32_16x16x32_bf16 v[0:3], v[84:87], v[220:223], v[0:3]
	s_barrier
	s_setprio 0
	s_add_u32 s50, s22, 0x80000
	s_addc_u32 s51, s23, 0
	s_add_i32 s49, s52, s31
	v_lshl_add_u64 v[68:69], s[50:51], 0, v[168:169]
	s_mov_b32 m0, s49
	s_nop 0
	global_load_lds_dwordx4 v[68:69], off
	v_lshl_add_u64 v[68:69], s[50:51], 0, v[156:157]
	s_add_i32 m0, s49, 0x2000
	s_nop 0
	global_load_lds_dwordx4 v[68:69], off
	s_waitcnt vmcnt(6)
	s_setprio 1
	s_barrier
	v_mfma_f32_16x16x32_bf16 v[52:55], v[224:227], v[144:147], v[52:55]
	v_mfma_f32_16x16x32_bf16 v[48:51], v[232:235], v[144:147], v[48:51]
	ds_read_b128 v[144:147], v183 offset:32768
	v_mfma_f32_16x16x32_bf16 v[36:39], v[224:227], v[172:175], v[36:39]
	v_mfma_f32_16x16x32_bf16 v[32:35], v[232:235], v[172:175], v[32:35]
	ds_read_b128 v[172:175], v183 offset:34816
	v_mfma_f32_16x16x32_bf16 v[24:27], v[224:227], v[208:211], v[24:27]
	v_mfma_f32_16x16x32_bf16 v[16:19], v[232:235], v[208:211], v[16:19]
	ds_read_b128 v[208:211], v183 offset:36864
	v_mfma_f32_16x16x32_bf16 v[12:15], v[224:227], v[216:219], v[12:15]
	v_mfma_f32_16x16x32_bf16 v[4:7], v[232:235], v[216:219], v[4:7]
	ds_read_b128 v[216:219], v183 offset:38912
	v_mfma_f32_16x16x32_bf16 v[52:55], v[228:231], v[148:151], v[52:55]
	v_mfma_f32_16x16x32_bf16 v[48:51], v[236:239], v[148:151], v[48:51]
	ds_read_b128 v[148:151], v183 offset:33792
	v_mfma_f32_16x16x32_bf16 v[36:39], v[228:231], v[176:179], v[36:39]
	v_mfma_f32_16x16x32_bf16 v[32:35], v[236:239], v[176:179], v[32:35]
	ds_read_b128 v[176:179], v183 offset:35840
	v_mfma_f32_16x16x32_bf16 v[24:27], v[228:231], v[212:215], v[24:27]
	v_mfma_f32_16x16x32_bf16 v[16:19], v[236:239], v[212:215], v[16:19]
	ds_read_b128 v[212:215], v183 offset:37888
	v_mfma_f32_16x16x32_bf16 v[12:15], v[228:231], v[220:223], v[12:15]
	v_mfma_f32_16x16x32_bf16 v[4:7], v[236:239], v[220:223], v[4:7]
	ds_read_b128 v[220:223], v183 offset:39936
	s_barrier
	s_setprio 0
	s_add_i32 s49, 0, 0x18000
	v_add_u32_e32 v84, s49, v181
	ds_read_b128 v[68:71], v84
	ds_read_b128 v[76:79], v84 offset:1024
	ds_read_b128 v[80:83], v84 offset:2048
	ds_read_b128 v[84:87], v84 offset:3072
	s_mov_b32 m0, s36
	v_lshl_add_u64 v[224:225], s[24:25], 0, v[154:155]
	global_load_lds_dwordx4 v[224:225], off
	v_lshl_add_u64 v[224:225], s[24:25], 0, v[160:161]
	s_mov_b32 m0, s37
	s_nop 0
	global_load_lds_dwordx4 v[224:225], off
	s_waitcnt lgkmcnt(0)
	s_setprio 1
	s_barrier
	s_waitcnt lgkmcnt(0)
	v_mfma_f32_16x16x32_bf16 v[140:143], v[68:71], v[144:147], v[140:143]
	v_mfma_f32_16x16x32_bf16 v[136:139], v[80:83], v[144:147], v[136:139]
	v_mfma_f32_16x16x32_bf16 v[124:127], v[68:71], v[172:175], v[124:127]
	v_mfma_f32_16x16x32_bf16 v[120:123], v[80:83], v[172:175], v[120:123]
	v_mfma_f32_16x16x32_bf16 v[108:111], v[68:71], v[208:211], v[108:111]
	v_mfma_f32_16x16x32_bf16 v[104:107], v[80:83], v[208:211], v[104:107]
	v_mfma_f32_16x16x32_bf16 v[92:95], v[68:71], v[216:219], v[92:95]
	v_mfma_f32_16x16x32_bf16 v[88:91], v[80:83], v[216:219], v[88:91]
	v_mfma_f32_16x16x32_bf16 v[140:143], v[76:79], v[148:151], v[140:143]
	v_mfma_f32_16x16x32_bf16 v[136:139], v[84:87], v[148:151], v[136:139]
	v_mfma_f32_16x16x32_bf16 v[124:127], v[76:79], v[176:179], v[124:127]
	v_mfma_f32_16x16x32_bf16 v[120:123], v[84:87], v[176:179], v[120:123]
	v_mfma_f32_16x16x32_bf16 v[108:111], v[76:79], v[212:215], v[108:111]
	v_mfma_f32_16x16x32_bf16 v[104:107], v[84:87], v[212:215], v[104:107]
	v_mfma_f32_16x16x32_bf16 v[92:95], v[76:79], v[220:223], v[92:95]
	v_mfma_f32_16x16x32_bf16 v[88:91], v[84:87], v[220:223], v[88:91]
	s_barrier
	s_setprio 0
	s_add_i32 s24, 0, 0x1c000
	s_add_i32 s25, s49, s31
	v_add_u32_e32 v170, s24, v181
	v_lshl_add_u64 v[166:167], v[166:167], 0, s[94:95]
	s_mov_b32 m0, s25
	ds_read_b128 v[224:227], v170
	ds_read_b128 v[228:231], v170 offset:1024
	ds_read_b128 v[232:235], v170 offset:2048
	ds_read_b128 v[236:239], v170 offset:3072
	global_load_lds_dwordx4 v[166:167], off
	v_lshl_add_u64 v[166:167], v[184:185], 0, s[94:95]
	s_add_i32 m0, s25, 0x2000
	s_nop 0
	global_load_lds_dwordx4 v[166:167], off
	s_setprio 1
	s_barrier
	s_waitcnt lgkmcnt(0)
	v_mfma_f32_16x16x32_bf16 v[132:135], v[224:227], v[144:147], v[132:135]
	v_mfma_f32_16x16x32_bf16 v[128:131], v[232:235], v[144:147], v[128:131]
	ds_read_b128 v[144:147], v183 offset:49152
	v_mfma_f32_16x16x32_bf16 v[116:119], v[224:227], v[172:175], v[116:119]
	v_mfma_f32_16x16x32_bf16 v[112:115], v[232:235], v[172:175], v[112:115]
	ds_read_b128 v[172:175], v183 offset:51200
	v_mfma_f32_16x16x32_bf16 v[100:103], v[224:227], v[208:211], v[100:103]
	v_mfma_f32_16x16x32_bf16 v[96:99], v[232:235], v[208:211], v[96:99]
	ds_read_b128 v[208:211], v183 offset:53248
	v_mfma_f32_16x16x32_bf16 v[72:75], v[224:227], v[216:219], v[72:75]
	v_mfma_f32_16x16x32_bf16 v[64:67], v[232:235], v[216:219], v[64:67]
	ds_read_b128 v[216:219], v183 offset:55296
	v_mfma_f32_16x16x32_bf16 v[132:135], v[228:231], v[148:151], v[132:135]
	v_mfma_f32_16x16x32_bf16 v[128:131], v[236:239], v[148:151], v[128:131]
	ds_read_b128 v[148:151], v183 offset:50176
	v_mfma_f32_16x16x32_bf16 v[116:119], v[228:231], v[176:179], v[116:119]
	v_mfma_f32_16x16x32_bf16 v[112:115], v[236:239], v[176:179], v[112:115]
	ds_read_b128 v[176:179], v183 offset:52224
	v_mfma_f32_16x16x32_bf16 v[100:103], v[228:231], v[212:215], v[100:103]
	v_mfma_f32_16x16x32_bf16 v[96:99], v[236:239], v[212:215], v[96:99]
	ds_read_b128 v[212:215], v183 offset:54272
	v_mfma_f32_16x16x32_bf16 v[72:75], v[228:231], v[220:223], v[72:75]
	v_mfma_f32_16x16x32_bf16 v[64:67], v[236:239], v[220:223], v[64:67]
	ds_read_b128 v[220:223], v183 offset:56320
	s_barrier
	s_setprio 0
	s_mov_b32 m0, s40
	v_lshl_add_u64 v[166:167], v[240:241], 0, s[94:95]
	global_load_lds_dwordx4 v[166:167], off
	v_lshl_add_u64 v[166:167], v[242:243], 0, s[94:95]
	s_mov_b32 m0, s41
	s_nop 0
	global_load_lds_dwordx4 v[166:167], off
	s_waitcnt vmcnt(8)
	s_setprio 1
	s_barrier
	s_waitcnt lgkmcnt(0)
	v_mfma_f32_16x16x32_bf16 v[60:63], v[68:71], v[144:147], v[60:63]
	v_mfma_f32_16x16x32_bf16 v[56:59], v[80:83], v[144:147], v[56:59]
	v_mfma_f32_16x16x32_bf16 v[44:47], v[68:71], v[172:175], v[44:47]
	v_mfma_f32_16x16x32_bf16 v[40:43], v[80:83], v[172:175], v[40:43]
	v_mfma_f32_16x16x32_bf16 v[28:31], v[68:71], v[208:211], v[28:31]
	v_mfma_f32_16x16x32_bf16 v[20:23], v[80:83], v[208:211], v[20:23]
	v_mfma_f32_16x16x32_bf16 v[8:11], v[68:71], v[216:219], v[8:11]
	v_mfma_f32_16x16x32_bf16 v[0:3], v[80:83], v[216:219], v[0:3]
	v_mfma_f32_16x16x32_bf16 v[60:63], v[76:79], v[148:151], v[60:63]
	v_mfma_f32_16x16x32_bf16 v[56:59], v[84:87], v[148:151], v[56:59]
	v_mfma_f32_16x16x32_bf16 v[44:47], v[76:79], v[176:179], v[44:47]
	v_mfma_f32_16x16x32_bf16 v[40:43], v[84:87], v[176:179], v[40:43]
	v_mfma_f32_16x16x32_bf16 v[28:31], v[76:79], v[212:215], v[28:31]
	v_mfma_f32_16x16x32_bf16 v[20:23], v[84:87], v[212:215], v[20:23]
	v_mfma_f32_16x16x32_bf16 v[8:11], v[76:79], v[220:223], v[8:11]
	v_mfma_f32_16x16x32_bf16 v[0:3], v[84:87], v[220:223], v[0:3]
	s_barrier
	s_setprio 0
	s_add_u32 s22, s22, 0x80080
	s_addc_u32 s23, s23, 0
	s_add_i32 s24, s24, s31
	v_lshl_add_u64 v[68:69], s[22:23], 0, v[168:169]
	s_mov_b32 m0, s24
	s_nop 0
	global_load_lds_dwordx4 v[68:69], off
	v_lshl_add_u64 v[68:69], s[22:23], 0, v[156:157]
	s_add_i32 m0, s24, 0x2000
	s_nop 0
	global_load_lds_dwordx4 v[68:69], off
	s_waitcnt vmcnt(6)
	s_setprio 1
	s_barrier
	v_mfma_f32_16x16x32_bf16 v[52:55], v[224:227], v[144:147], v[52:55]
	v_mfma_f32_16x16x32_bf16 v[48:51], v[232:235], v[144:147], v[48:51]
	ds_read_b128 v[144:147], v183
	v_mfma_f32_16x16x32_bf16 v[36:39], v[224:227], v[172:175], v[36:39]
	v_mfma_f32_16x16x32_bf16 v[32:35], v[232:235], v[172:175], v[32:35]
	ds_read_b128 v[172:175], v183 offset:2048
	v_mfma_f32_16x16x32_bf16 v[24:27], v[224:227], v[208:211], v[24:27]
	v_mfma_f32_16x16x32_bf16 v[16:19], v[232:235], v[208:211], v[16:19]
	ds_read_b128 v[208:211], v183 offset:4096
	v_mfma_f32_16x16x32_bf16 v[12:15], v[224:227], v[216:219], v[12:15]
	v_mfma_f32_16x16x32_bf16 v[4:7], v[232:235], v[216:219], v[4:7]
	ds_read_b128 v[216:219], v183 offset:6144
	v_mfma_f32_16x16x32_bf16 v[52:55], v[228:231], v[148:151], v[52:55]
	v_mfma_f32_16x16x32_bf16 v[48:51], v[236:239], v[148:151], v[48:51]
	ds_read_b128 v[148:151], v183 offset:1024
	v_mfma_f32_16x16x32_bf16 v[36:39], v[228:231], v[176:179], v[36:39]
	v_mfma_f32_16x16x32_bf16 v[32:35], v[236:239], v[176:179], v[32:35]
	ds_read_b128 v[176:179], v183 offset:3072
	v_mfma_f32_16x16x32_bf16 v[24:27], v[228:231], v[212:215], v[24:27]
	v_mfma_f32_16x16x32_bf16 v[16:19], v[236:239], v[212:215], v[16:19]
	ds_read_b128 v[212:215], v183 offset:5120
	v_mfma_f32_16x16x32_bf16 v[12:15], v[228:231], v[220:223], v[12:15]
	v_mfma_f32_16x16x32_bf16 v[4:7], v[236:239], v[220:223], v[4:7]
	ds_read_b128 v[220:223], v183 offset:7168
	s_barrier
	s_setprio 0
	s_add_i32 s48, s48, 2
	s_add_u32 s4, s4, 0x100
	s_addc_u32 s5, s5, 0
	s_add_u32 s46, s46, 0x100
	s_addc_u32 s47, s47, 0
	s_cmp_gt_u32 s48, 29
	s_cbranch_scc0 .LBB0_1002
	s_waitcnt lgkmcnt(0)
	s_and_b64 vcc, exec, s[14:15]
	s_cbranch_vccz .LBB0_1005
	s_barrier

.LBB0_1422:
	s_add_u32 s23, s34, 0x100
	s_addc_u32 s56, s35, 0
	s_add_u32 s34, s26, 0x80
	v_mov_b32_e32 v129, v169
	v_mov_b32_e32 v139, v169
	s_addc_u32 s35, s27, 0
	v_lshl_add_u64 v[142:143], s[34:35], 0, v[138:139]
	v_lshl_add_u64 v[144:145], s[34:35], 0, v[128:129]
	s_mov_b32 s57, -2
	s_mov_b64 s[34:35], 0
	ds_read_b128 v[180:183], v152
	ds_read_b128 v[208:211], v152 offset:1024
	ds_read_b128 v[212:215], v152 offset:2048
	ds_read_b128 v[216:219], v152 offset:3072
	ds_read_b128 v[220:223], v152 offset:4096
	ds_read_b128 v[224:227], v152 offset:5120
	ds_read_b128 v[228:231], v152 offset:6144
	ds_read_b128 v[232:235], v152 offset:7168
.LBB0_1423:
	s_add_u32 s36, s26, s34
	s_addc_u32 s37, s27, s35
	s_add_u32 s38, s36, 0x100
	s_addc_u32 s39, s37, 0
	s_add_u32 s58, s23, s34
	s_addc_u32 s59, s56, s35
	s_add_i32 s60, 0, 0x10000
	v_add_u32_e32 v141, s60, v135
	ds_read_b128 v[158:161], v141
	ds_read_b128 v[162:165], v141 offset:1024
	ds_read_b128 v[172:175], v141 offset:2048
	ds_read_b128 v[176:179], v141 offset:3072
	s_cmpk_eq_i32 s34, 0xf00
	s_cselect_b64 vcc, -1, 0
	s_and_b64 s[36:37], vcc, exec
	v_cndmask_b32_e32 v168, v134, v154, vcc
	v_cndmask_b32_e32 v166, v132, v155, vcc
	v_cndmask_b32_e32 v129, v128, v153, vcc
	v_cndmask_b32_e32 v139, v138, v156, vcc
	s_cselect_b32 s39, s31, s39
	s_cselect_b32 s38, s30, s38
	s_cselect_b32 s37, s5, s59
	s_cselect_b32 s36, s4, s58
	v_lshl_add_u64 v[184:185], v[144:145], 0, s[34:35]
	s_add_i32 m0, s43, 0xc000
	s_nop 0
	global_load_lds_dwordx4 v[184:185], off
	v_lshl_add_u64 v[184:185], v[142:143], 0, s[34:35]
	s_add_i32 m0, s43, 0xe000
	s_nop 0
	global_load_lds_dwordx4 v[184:185], off
	s_waitcnt lgkmcnt(0)
	s_setprio 1
	s_barrier
	s_waitcnt lgkmcnt(0)
	v_mfma_f32_16x16x32_bf16 v[124:127], v[158:161], v[180:183], v[124:127]
	v_mfma_f32_16x16x32_bf16 v[120:123], v[172:175], v[180:183], v[120:123]
	v_mfma_f32_16x16x32_bf16 v[116:119], v[158:161], v[212:215], v[116:119]
	v_mfma_f32_16x16x32_bf16 v[112:115], v[172:175], v[212:215], v[112:115]
	v_mfma_f32_16x16x32_bf16 v[108:111], v[158:161], v[220:223], v[108:111]
	v_mfma_f32_16x16x32_bf16 v[104:107], v[172:175], v[220:223], v[104:107]
	v_mfma_f32_16x16x32_bf16 v[100:103], v[158:161], v[228:231], v[100:103]
	v_mfma_f32_16x16x32_bf16 v[96:99], v[172:175], v[228:231], v[96:99]
	v_mfma_f32_16x16x32_bf16 v[124:127], v[162:165], v[208:211], v[124:127]
	v_mfma_f32_16x16x32_bf16 v[120:123], v[176:179], v[208:211], v[120:123]
	v_mfma_f32_16x16x32_bf16 v[116:119], v[162:165], v[216:219], v[116:119]
	v_mfma_f32_16x16x32_bf16 v[112:115], v[176:179], v[216:219], v[112:115]
	v_mfma_f32_16x16x32_bf16 v[108:111], v[162:165], v[224:227], v[108:111]
	v_mfma_f32_16x16x32_bf16 v[104:107], v[176:179], v[224:227], v[104:107]
	v_mfma_f32_16x16x32_bf16 v[100:103], v[162:165], v[232:235], v[100:103]
	v_mfma_f32_16x16x32_bf16 v[96:99], v[176:179], v[232:235], v[96:99]
	s_barrier
	s_setprio 0
	s_add_i32 s61, 0, 0x14000
	s_add_i32 s58, s60, s9
	v_add_u32_e32 v141, s61, v135
	v_lshl_add_u64 v[184:185], s[36:37], 0, v[130:131]
	s_mov_b32 m0, s58
	ds_read_b128 v[236:239], v141
	ds_read_b128 v[240:243], v141 offset:1024
	ds_read_b128 v[244:247], v141 offset:2048
	ds_read_b128 v[248:251], v141 offset:3072
	global_load_lds_dwordx4 v[184:185], off
	v_lshl_add_u64 v[188:189], s[36:37], 0, v[136:137]
	s_add_i32 m0, s58, 0x2000
	s_nop 0
	global_load_lds_dwordx4 v[188:189], off
	s_setprio 1
	s_barrier
	s_waitcnt lgkmcnt(0)
	v_mfma_f32_16x16x32_bf16 v[92:95], v[236:239], v[180:183], v[92:95]
	v_mfma_f32_16x16x32_bf16 v[88:91], v[244:247], v[180:183], v[88:91]
	ds_read_b128 v[180:183], v152 offset:16384
	v_mfma_f32_16x16x32_bf16 v[84:87], v[236:239], v[212:215], v[84:87]
	v_mfma_f32_16x16x32_bf16 v[80:83], v[244:247], v[212:215], v[80:83]
	ds_read_b128 v[212:215], v152 offset:18432
	v_mfma_f32_16x16x32_bf16 v[76:79], v[236:239], v[220:223], v[76:79]
	v_mfma_f32_16x16x32_bf16 v[72:75], v[244:247], v[220:223], v[72:75]
	ds_read_b128 v[220:223], v152 offset:20480
	v_mfma_f32_16x16x32_bf16 v[68:71], v[236:239], v[228:231], v[68:71]
	v_mfma_f32_16x16x32_bf16 v[64:67], v[244:247], v[228:231], v[64:67]
	ds_read_b128 v[228:231], v152 offset:22528
	v_mfma_f32_16x16x32_bf16 v[92:95], v[240:243], v[208:211], v[92:95]
	v_mfma_f32_16x16x32_bf16 v[88:91], v[248:251], v[208:211], v[88:91]
	ds_read_b128 v[208:211], v152 offset:17408
	v_mfma_f32_16x16x32_bf16 v[84:87], v[240:243], v[216:219], v[84:87]
	v_mfma_f32_16x16x32_bf16 v[80:83], v[248:251], v[216:219], v[80:83]
	ds_read_b128 v[216:219], v152 offset:19456
	v_mfma_f32_16x16x32_bf16 v[76:79], v[240:243], v[224:227], v[76:79]
	v_mfma_f32_16x16x32_bf16 v[72:75], v[248:251], v[224:227], v[72:75]
	ds_read_b128 v[224:227], v152 offset:21504
	v_mfma_f32_16x16x32_bf16 v[68:71], v[240:243], v[232:235], v[68:71]
	v_mfma_f32_16x16x32_bf16 v[64:67], v[248:251], v[232:235], v[64:67]
	ds_read_b128 v[232:235], v152 offset:23552
	s_barrier
	s_setprio 0
	s_mov_b32 m0, s43
	s_nop 0
	global_load_lds_dwordx4 v168, s[38:39]
	s_mov_b32 m0, s44
	v_mov_b32_e32 v167, v169
	global_load_lds_dwordx4 v166, s[38:39]
	s_waitcnt vmcnt(8)
	v_lshl_add_u64 v[170:171], s[38:39], 0, v[168:169]
	v_lshl_add_u64 v[166:167], s[38:39], 0, v[166:167]
	s_setprio 1
	s_barrier
	s_waitcnt lgkmcnt(0)
	v_mfma_f32_16x16x32_bf16 v[60:63], v[158:161], v[180:183], v[60:63]
	v_mfma_f32_16x16x32_bf16 v[56:59], v[172:175], v[180:183], v[56:59]
	v_mfma_f32_16x16x32_bf16 v[52:55], v[158:161], v[212:215], v[52:55]
	v_mfma_f32_16x16x32_bf16 v[48:51], v[172:175], v[212:215], v[48:51]
	v_mfma_f32_16x16x32_bf16 v[44:47], v[158:161], v[220:223], v[44:47]
	v_mfma_f32_16x16x32_bf16 v[40:43], v[172:175], v[220:223], v[40:43]
	v_mfma_f32_16x16x32_bf16 v[36:39], v[158:161], v[228:231], v[36:39]
	v_mfma_f32_16x16x32_bf16 v[32:35], v[172:175], v[228:231], v[32:35]
	v_mfma_f32_16x16x32_bf16 v[60:63], v[162:165], v[208:211], v[60:63]
	v_mfma_f32_16x16x32_bf16 v[56:59], v[176:179], v[208:211], v[56:59]
	v_mfma_f32_16x16x32_bf16 v[52:55], v[162:165], v[216:219], v[52:55]
	v_mfma_f32_16x16x32_bf16 v[48:51], v[176:179], v[216:219], v[48:51]
	v_mfma_f32_16x16x32_bf16 v[44:47], v[162:165], v[224:227], v[44:47]
	v_mfma_f32_16x16x32_bf16 v[40:43], v[176:179], v[224:227], v[40:43]
	v_mfma_f32_16x16x32_bf16 v[36:39], v[162:165], v[232:235], v[36:39]
	v_mfma_f32_16x16x32_bf16 v[32:35], v[176:179], v[232:235], v[32:35]
	s_barrier
	s_setprio 0
	s_add_u32 s58, s36, 0x80000
	s_addc_u32 s59, s37, 0
	s_add_i32 s60, s61, s9
	v_lshl_add_u64 v[158:159], s[58:59], 0, v[130:131]
	s_mov_b32 m0, s60
	s_nop 0
	global_load_lds_dwordx4 v[158:159], off
	v_lshl_add_u64 v[158:159], s[58:59], 0, v[136:137]
	s_add_i32 m0, s60, 0x2000
	s_nop 0
	global_load_lds_dwordx4 v[158:159], off
	s_waitcnt vmcnt(6)
	s_setprio 1
	s_barrier
	v_mfma_f32_16x16x32_bf16 v[28:31], v[236:239], v[180:183], v[28:31]
	v_mfma_f32_16x16x32_bf16 v[24:27], v[244:247], v[180:183], v[24:27]
	ds_read_b128 v[180:183], v152 offset:32768
	v_mfma_f32_16x16x32_bf16 v[20:23], v[236:239], v[212:215], v[20:23]
	v_mfma_f32_16x16x32_bf16 v[16:19], v[244:247], v[212:215], v[16:19]
	ds_read_b128 v[212:215], v152 offset:34816
	v_mfma_f32_16x16x32_bf16 v[12:15], v[236:239], v[220:223], v[12:15]
	v_mfma_f32_16x16x32_bf16 v[8:11], v[244:247], v[220:223], v[8:11]
	ds_read_b128 v[220:223], v152 offset:36864
	v_mfma_f32_16x16x32_bf16 v[4:7], v[236:239], v[228:231], v[4:7]
	v_mfma_f32_16x16x32_bf16 v[0:3], v[244:247], v[228:231], v[0:3]
	ds_read_b128 v[228:231], v152 offset:38912
	v_mfma_f32_16x16x32_bf16 v[28:31], v[240:243], v[208:211], v[28:31]
	v_mfma_f32_16x16x32_bf16 v[24:27], v[248:251], v[208:211], v[24:27]
	ds_read_b128 v[208:211], v152 offset:33792
	v_mfma_f32_16x16x32_bf16 v[20:23], v[240:243], v[216:219], v[20:23]
	v_mfma_f32_16x16x32_bf16 v[16:19], v[248:251], v[216:219], v[16:19]
	ds_read_b128 v[216:219], v152 offset:35840
	v_mfma_f32_16x16x32_bf16 v[12:15], v[240:243], v[224:227], v[12:15]
	v_mfma_f32_16x16x32_bf16 v[8:11], v[248:251], v[224:227], v[8:11]
	ds_read_b128 v[224:227], v152 offset:37888
	v_mfma_f32_16x16x32_bf16 v[4:7], v[240:243], v[232:235], v[4:7]
	v_mfma_f32_16x16x32_bf16 v[0:3], v[248:251], v[232:235], v[0:3]
	ds_read_b128 v[232:235], v152 offset:39936
	s_barrier
	s_setprio 0
	s_add_i32 s58, 0, 0x18000
	v_add_u32_e32 v141, s58, v135
	ds_read_b128 v[158:161], v141
	ds_read_b128 v[162:165], v141 offset:1024
	ds_read_b128 v[172:175], v141 offset:2048
	ds_read_b128 v[176:179], v141 offset:3072
	s_mov_b32 m0, s45
	s_nop 0
	global_load_lds_dwordx4 v129, s[38:39]
	s_mov_b32 m0, s46
	s_nop 0
	global_load_lds_dwordx4 v139, s[38:39]
	s_waitcnt lgkmcnt(0)
	s_setprio 1
	s_barrier
	s_waitcnt lgkmcnt(0)
	v_mfma_f32_16x16x32_bf16 v[124:127], v[158:161], v[180:183], v[124:127]
	v_mfma_f32_16x16x32_bf16 v[120:123], v[172:175], v[180:183], v[120:123]
	v_mfma_f32_16x16x32_bf16 v[116:119], v[158:161], v[212:215], v[116:119]
	v_mfma_f32_16x16x32_bf16 v[112:115], v[172:175], v[212:215], v[112:115]
	v_mfma_f32_16x16x32_bf16 v[108:111], v[158:161], v[220:223], v[108:111]
	v_mfma_f32_16x16x32_bf16 v[104:107], v[172:175], v[220:223], v[104:107]
	v_mfma_f32_16x16x32_bf16 v[100:103], v[158:161], v[228:231], v[100:103]
	v_mfma_f32_16x16x32_bf16 v[96:99], v[172:175], v[228:231], v[96:99]
	v_mfma_f32_16x16x32_bf16 v[124:127], v[162:165], v[208:211], v[124:127]
	v_mfma_f32_16x16x32_bf16 v[120:123], v[176:179], v[208:211], v[120:123]
	v_mfma_f32_16x16x32_bf16 v[116:119], v[162:165], v[216:219], v[116:119]
	v_mfma_f32_16x16x32_bf16 v[112:115], v[176:179], v[216:219], v[112:115]
	v_mfma_f32_16x16x32_bf16 v[108:111], v[162:165], v[224:227], v[108:111]
	v_mfma_f32_16x16x32_bf16 v[104:107], v[176:179], v[224:227], v[104:107]
	v_mfma_f32_16x16x32_bf16 v[100:103], v[162:165], v[232:235], v[100:103]
	v_mfma_f32_16x16x32_bf16 v[96:99], v[176:179], v[232:235], v[96:99]
	s_barrier
	s_setprio 0
	s_add_i32 s38, 0, 0x1c000
	s_add_i32 s39, s58, s9
	v_add_u32_e32 v129, s38, v135
	v_lshl_add_u64 v[184:185], v[184:185], 0, s[94:95]
	s_mov_b32 m0, s39
	ds_read_b128 v[236:239], v129
	ds_read_b128 v[240:243], v129 offset:1024
	ds_read_b128 v[244:247], v129 offset:2048
	ds_read_b128 v[248:251], v129 offset:3072
	global_load_lds_dwordx4 v[184:185], off
	v_lshl_add_u64 v[184:185], v[188:189], 0, s[94:95]
	s_add_i32 m0, s39, 0x2000
	s_nop 0
	global_load_lds_dwordx4 v[184:185], off
	s_setprio 1
	s_barrier
	s_waitcnt lgkmcnt(0)
	v_mfma_f32_16x16x32_bf16 v[92:95], v[236:239], v[180:183], v[92:95]
	v_mfma_f32_16x16x32_bf16 v[88:91], v[244:247], v[180:183], v[88:91]
	ds_read_b128 v[180:183], v152 offset:49152
	v_mfma_f32_16x16x32_bf16 v[84:87], v[236:239], v[212:215], v[84:87]
	v_mfma_f32_16x16x32_bf16 v[80:83], v[244:247], v[212:215], v[80:83]
	ds_read_b128 v[212:215], v152 offset:51200
	v_mfma_f32_16x16x32_bf16 v[76:79], v[236:239], v[220:223], v[76:79]
	v_mfma_f32_16x16x32_bf16 v[72:75], v[244:247], v[220:223], v[72:75]
	ds_read_b128 v[220:223], v152 offset:53248
	v_mfma_f32_16x16x32_bf16 v[68:71], v[236:239], v[228:231], v[68:71]
	v_mfma_f32_16x16x32_bf16 v[64:67], v[244:247], v[228:231], v[64:67]
	ds_read_b128 v[228:231], v152 offset:55296
	v_mfma_f32_16x16x32_bf16 v[92:95], v[240:243], v[208:211], v[92:95]
	v_mfma_f32_16x16x32_bf16 v[88:91], v[248:251], v[208:211], v[88:91]
	ds_read_b128 v[208:211], v152 offset:50176
	v_mfma_f32_16x16x32_bf16 v[84:87], v[240:243], v[216:219], v[84:87]
	v_mfma_f32_16x16x32_bf16 v[80:83], v[248:251], v[216:219], v[80:83]
	ds_read_b128 v[216:219], v152 offset:52224
	v_mfma_f32_16x16x32_bf16 v[76:79], v[240:243], v[224:227], v[76:79]
	v_mfma_f32_16x16x32_bf16 v[72:75], v[248:251], v[224:227], v[72:75]
	ds_read_b128 v[224:227], v152 offset:54272
	v_mfma_f32_16x16x32_bf16 v[68:71], v[240:243], v[232:235], v[68:71]
	v_mfma_f32_16x16x32_bf16 v[64:67], v[248:251], v[232:235], v[64:67]
	ds_read_b128 v[232:235], v152 offset:56320
	s_barrier
	s_setprio 0
	s_mov_b32 m0, s47
	v_lshl_add_u64 v[170:171], v[170:171], 0, s[94:95]
	global_load_lds_dwordx4 v[170:171], off
	v_lshl_add_u64 v[166:167], v[166:167], 0, s[94:95]
	s_mov_b32 m0, s48
	s_nop 0
	global_load_lds_dwordx4 v[166:167], off
	s_waitcnt vmcnt(8)
	s_setprio 1
	s_barrier
	s_waitcnt lgkmcnt(0)
	v_mfma_f32_16x16x32_bf16 v[60:63], v[158:161], v[180:183], v[60:63]
	v_mfma_f32_16x16x32_bf16 v[56:59], v[172:175], v[180:183], v[56:59]
	v_mfma_f32_16x16x32_bf16 v[52:55], v[158:161], v[212:215], v[52:55]
	v_mfma_f32_16x16x32_bf16 v[48:51], v[172:175], v[212:215], v[48:51]
	v_mfma_f32_16x16x32_bf16 v[44:47], v[158:161], v[220:223], v[44:47]
	v_mfma_f32_16x16x32_bf16 v[40:43], v[172:175], v[220:223], v[40:43]
	v_mfma_f32_16x16x32_bf16 v[36:39], v[158:161], v[228:231], v[36:39]
	v_mfma_f32_16x16x32_bf16 v[32:35], v[172:175], v[228:231], v[32:35]
	v_mfma_f32_16x16x32_bf16 v[60:63], v[162:165], v[208:211], v[60:63]
	v_mfma_f32_16x16x32_bf16 v[56:59], v[176:179], v[208:211], v[56:59]
	v_mfma_f32_16x16x32_bf16 v[52:55], v[162:165], v[216:219], v[52:55]
	v_mfma_f32_16x16x32_bf16 v[48:51], v[176:179], v[216:219], v[48:51]
	v_mfma_f32_16x16x32_bf16 v[44:47], v[162:165], v[224:227], v[44:47]
	v_mfma_f32_16x16x32_bf16 v[40:43], v[176:179], v[224:227], v[40:43]
	v_mfma_f32_16x16x32_bf16 v[36:39], v[162:165], v[232:235], v[36:39]
	v_mfma_f32_16x16x32_bf16 v[32:35], v[176:179], v[232:235], v[32:35]
	s_barrier
	s_setprio 0
	s_add_u32 s36, s36, 0x80080
	s_addc_u32 s37, s37, 0
	s_add_i32 s38, s38, s9
	v_lshl_add_u64 v[158:159], s[36:37], 0, v[130:131]
	s_mov_b32 m0, s38
	s_nop 0
	global_load_lds_dwordx4 v[158:159], off
	v_lshl_add_u64 v[158:159], s[36:37], 0, v[136:137]
	s_add_i32 m0, s38, 0x2000
	s_nop 0
	global_load_lds_dwordx4 v[158:159], off
	s_waitcnt vmcnt(6)
	s_setprio 1
	s_barrier
	v_mfma_f32_16x16x32_bf16 v[28:31], v[236:239], v[180:183], v[28:31]
	v_mfma_f32_16x16x32_bf16 v[24:27], v[244:247], v[180:183], v[24:27]
	ds_read_b128 v[180:183], v152
	v_mfma_f32_16x16x32_bf16 v[20:23], v[236:239], v[212:215], v[20:23]
	v_mfma_f32_16x16x32_bf16 v[16:19], v[244:247], v[212:215], v[16:19]
	ds_read_b128 v[212:215], v152 offset:2048
	v_mfma_f32_16x16x32_bf16 v[12:15], v[236:239], v[220:223], v[12:15]
	v_mfma_f32_16x16x32_bf16 v[8:11], v[244:247], v[220:223], v[8:11]
	ds_read_b128 v[220:223], v152 offset:4096
	v_mfma_f32_16x16x32_bf16 v[4:7], v[236:239], v[228:231], v[4:7]
	v_mfma_f32_16x16x32_bf16 v[0:3], v[244:247], v[228:231], v[0:3]
	ds_read_b128 v[228:231], v152 offset:6144
	v_mfma_f32_16x16x32_bf16 v[28:31], v[240:243], v[208:211], v[28:31]
	v_mfma_f32_16x16x32_bf16 v[24:27], v[248:251], v[208:211], v[24:27]
	ds_read_b128 v[208:211], v152 offset:1024
	v_mfma_f32_16x16x32_bf16 v[20:23], v[240:243], v[216:219], v[20:23]
	v_mfma_f32_16x16x32_bf16 v[16:19], v[248:251], v[216:219], v[16:19]
	ds_read_b128 v[216:219], v152 offset:3072
	v_mfma_f32_16x16x32_bf16 v[12:15], v[240:243], v[224:227], v[12:15]
	v_mfma_f32_16x16x32_bf16 v[8:11], v[248:251], v[224:227], v[8:11]
	ds_read_b128 v[224:227], v152 offset:5120
	v_mfma_f32_16x16x32_bf16 v[4:7], v[240:243], v[232:235], v[4:7]
	v_mfma_f32_16x16x32_bf16 v[0:3], v[248:251], v[232:235], v[0:3]
	ds_read_b128 v[232:235], v152 offset:7168
	s_barrier
	s_setprio 0
	s_add_i32 s57, s57, 2
	s_add_u32 s34, s34, 0x100
	s_addc_u32 s35, s35, 0
	s_cmp_gt_u32 s57, 29
	s_cbranch_scc0 .LBB0_1423
	s_waitcnt lgkmcnt(0)
	s_and_b64 vcc, exec, s[16:17]
	s_cbranch_vccz .LBB0_1426
	s_barrier

.LBB0_1520:
	s_and_b64 s[28:29], s[22:23], exec
	s_cselect_b32 s17, s15, s25
	s_cselect_b32 s21, s14, s24
	s_cselect_b32 s30, s19, s27
	s_cselect_b32 s31, s18, s26
	s_add_u32 s24, s24, 0x80
	s_addc_u32 s25, s25, 0
	s_add_u32 s34, s26, 0x100
	v_mov_b32_e32 v8, 0
	s_addc_u32 s35, s27, 0
	s_mov_b32 s56, -2
	v_mov_b32_e32 v9, v8
	v_mov_b32_e32 v10, v8
	v_mov_b32_e32 v11, v8
	v_mov_b32_e32 v20, v8
	v_mov_b32_e32 v21, v8
	v_mov_b32_e32 v22, v8
	v_mov_b32_e32 v23, v8
	v_mov_b32_e32 v36, v8
	v_mov_b32_e32 v37, v8
	v_mov_b32_e32 v38, v8
	v_mov_b32_e32 v39, v8
	v_mov_b32_e32 v44, v8
	v_mov_b32_e32 v45, v8
	v_mov_b32_e32 v46, v8
	v_mov_b32_e32 v47, v8
	v_mov_b32_e32 v0, v8
	v_mov_b32_e32 v1, v8
	v_mov_b32_e32 v2, v8
	v_mov_b32_e32 v3, v8
	v_mov_b32_e32 v4, v8
	v_mov_b32_e32 v5, v8
	v_mov_b32_e32 v6, v8
	v_mov_b32_e32 v7, v8
	v_mov_b32_e32 v12, v8
	v_mov_b32_e32 v13, v8
	v_mov_b32_e32 v14, v8
	v_mov_b32_e32 v15, v8
	v_mov_b32_e32 v16, v8
	v_mov_b32_e32 v17, v8
	v_mov_b32_e32 v18, v8
	v_mov_b32_e32 v19, v8
	v_mov_b32_e32 v32, v8
	v_mov_b32_e32 v33, v8
	v_mov_b32_e32 v34, v8
	v_mov_b32_e32 v35, v8
	v_mov_b32_e32 v40, v8
	v_mov_b32_e32 v41, v8
	v_mov_b32_e32 v42, v8
	v_mov_b32_e32 v43, v8
	v_mov_b32_e32 v56, v8
	v_mov_b32_e32 v57, v8
	v_mov_b32_e32 v58, v8
	v_mov_b32_e32 v59, v8
	v_mov_b32_e32 v60, v8
	v_mov_b32_e32 v61, v8
	v_mov_b32_e32 v62, v8
	v_mov_b32_e32 v63, v8
	v_mov_b32_e32 v64, v8
	v_mov_b32_e32 v65, v8
	v_mov_b32_e32 v66, v8
	v_mov_b32_e32 v67, v8
	v_mov_b32_e32 v68, v8
	v_mov_b32_e32 v69, v8
	v_mov_b32_e32 v70, v8
	v_mov_b32_e32 v71, v8
	v_mov_b32_e32 v76, v8
	v_mov_b32_e32 v77, v8
	v_mov_b32_e32 v78, v8
	v_mov_b32_e32 v79, v8
	v_mov_b32_e32 v84, v8
	v_mov_b32_e32 v85, v8
	v_mov_b32_e32 v86, v8
	v_mov_b32_e32 v87, v8
	v_mov_b32_e32 v92, v8
	v_mov_b32_e32 v93, v8
	v_mov_b32_e32 v94, v8
	v_mov_b32_e32 v95, v8
	v_mov_b32_e32 v100, v8
	v_mov_b32_e32 v101, v8
	v_mov_b32_e32 v102, v8
	v_mov_b32_e32 v103, v8
	v_mov_b32_e32 v108, v8
	v_mov_b32_e32 v109, v8
	v_mov_b32_e32 v110, v8
	v_mov_b32_e32 v111, v8
	v_mov_b32_e32 v116, v8
	v_mov_b32_e32 v117, v8
	v_mov_b32_e32 v118, v8
	v_mov_b32_e32 v119, v8
	v_mov_b32_e32 v72, v8
	v_mov_b32_e32 v73, v8
	v_mov_b32_e32 v74, v8
	v_mov_b32_e32 v75, v8
	v_mov_b32_e32 v80, v8
	v_mov_b32_e32 v81, v8
	v_mov_b32_e32 v82, v8
	v_mov_b32_e32 v83, v8
	v_mov_b32_e32 v88, v8
	v_mov_b32_e32 v89, v8
	v_mov_b32_e32 v90, v8
	v_mov_b32_e32 v91, v8
	v_mov_b32_e32 v96, v8
	v_mov_b32_e32 v97, v8
	v_mov_b32_e32 v98, v8
	v_mov_b32_e32 v99, v8
	v_mov_b32_e32 v104, v8
	v_mov_b32_e32 v105, v8
	v_mov_b32_e32 v106, v8
	v_mov_b32_e32 v107, v8
	v_mov_b32_e32 v112, v8
	v_mov_b32_e32 v113, v8
	v_mov_b32_e32 v114, v8
	v_mov_b32_e32 v115, v8
	v_mov_b32_e32 v120, v8
	v_mov_b32_e32 v121, v8
	v_mov_b32_e32 v122, v8
	v_mov_b32_e32 v123, v8
	v_mov_b32_e32 v124, v8
	v_mov_b32_e32 v125, v8
	v_mov_b32_e32 v126, v8
	v_mov_b32_e32 v127, v8
	v_mov_b32_e32 v52, v8
	v_mov_b32_e32 v53, v8
	v_mov_b32_e32 v54, v8
	v_mov_b32_e32 v55, v8
	v_mov_b32_e32 v48, v8
	v_mov_b32_e32 v49, v8
	v_mov_b32_e32 v50, v8
	v_mov_b32_e32 v51, v8
	v_mov_b32_e32 v28, v8
	v_mov_b32_e32 v29, v8
	v_mov_b32_e32 v30, v8
	v_mov_b32_e32 v31, v8
	v_mov_b32_e32 v24, v8
	v_mov_b32_e32 v25, v8
	v_mov_b32_e32 v26, v8
	v_mov_b32_e32 v27, v8
	ds_read_b128 v[164:167], v146
	ds_read_b128 v[172:175], v146 offset:1024
	ds_read_b128 v[176:179], v146 offset:2048
	ds_read_b128 v[180:183], v146 offset:3072
	ds_read_b128 v[208:211], v146 offset:4096
	ds_read_b128 v[212:215], v146 offset:5120
	ds_read_b128 v[216:219], v146 offset:6144
	ds_read_b128 v[220:223], v146 offset:7168
.LBB0_1521:
	s_add_u32 s26, s24, 0x80
	s_addc_u32 s27, s25, 0
	s_add_i32 s57, 0, 0x10000
	v_add_u32_e32 v147, s57, v145
	ds_read_b128 v[148:151], v147
	ds_read_b128 v[152:155], v147 offset:1024
	ds_read_b128 v[156:159], v147 offset:2048
	ds_read_b128 v[160:163], v147 offset:3072
	s_cmp_eq_u32 s56, 4
	s_cselect_b32 s29, s17, s27
	s_cselect_b32 s28, s21, s26
	s_cselect_b32 s27, s30, s35
	s_cselect_b32 s26, s31, s34
	v_lshl_add_u64 v[170:171], s[24:25], 0, v[142:143]
	s_add_i32 m0, s43, 0xc000
	s_nop 0
	global_load_lds_dwordx4 v[170:171], off
	v_lshl_add_u64 v[170:171], s[24:25], 0, v[140:141]
	s_add_i32 m0, s43, 0xe000
	s_nop 0
	global_load_lds_dwordx4 v[170:171], off
	s_waitcnt lgkmcnt(0)
	s_setprio 1
	s_barrier
	s_waitcnt lgkmcnt(0)
	v_mfma_f32_16x16x32_bf16 v[124:127], v[148:151], v[164:167], v[124:127]
	v_mfma_f32_16x16x32_bf16 v[120:123], v[156:159], v[164:167], v[120:123]
	v_mfma_f32_16x16x32_bf16 v[112:115], v[148:151], v[176:179], v[112:115]
	v_mfma_f32_16x16x32_bf16 v[104:107], v[156:159], v[176:179], v[104:107]
	v_mfma_f32_16x16x32_bf16 v[96:99], v[148:151], v[208:211], v[96:99]
	v_mfma_f32_16x16x32_bf16 v[88:91], v[156:159], v[208:211], v[88:91]
	v_mfma_f32_16x16x32_bf16 v[80:83], v[148:151], v[216:219], v[80:83]
	v_mfma_f32_16x16x32_bf16 v[72:75], v[156:159], v[216:219], v[72:75]
	v_mfma_f32_16x16x32_bf16 v[124:127], v[152:155], v[172:175], v[124:127]
	v_mfma_f32_16x16x32_bf16 v[120:123], v[160:163], v[172:175], v[120:123]
	v_mfma_f32_16x16x32_bf16 v[112:115], v[152:155], v[180:183], v[112:115]
	v_mfma_f32_16x16x32_bf16 v[104:107], v[160:163], v[180:183], v[104:107]
	v_mfma_f32_16x16x32_bf16 v[96:99], v[152:155], v[212:215], v[96:99]
	v_mfma_f32_16x16x32_bf16 v[88:91], v[160:163], v[212:215], v[88:91]
	v_mfma_f32_16x16x32_bf16 v[80:83], v[152:155], v[220:223], v[80:83]
	v_mfma_f32_16x16x32_bf16 v[72:75], v[160:163], v[220:223], v[72:75]
	s_barrier
	s_setprio 0
	s_add_i32 s60, 0, 0x14000
	s_add_i32 s57, s57, s42
	v_add_u32_e32 v147, s60, v145
	v_lshl_add_u64 v[170:171], s[26:27], 0, v[168:169]
	s_mov_b32 m0, s57
	ds_read_b128 v[224:227], v147
	ds_read_b128 v[228:231], v147 offset:1024
	ds_read_b128 v[232:235], v147 offset:2048
	ds_read_b128 v[236:239], v147 offset:3072
	global_load_lds_dwordx4 v[170:171], off
	v_lshl_add_u64 v[184:185], s[26:27], 0, v[132:133]
	s_add_i32 m0, s57, 0x2000
	s_nop 0
	global_load_lds_dwordx4 v[184:185], off
	s_setprio 1
	s_barrier
	s_waitcnt lgkmcnt(0)
	v_mfma_f32_16x16x32_bf16 v[116:119], v[224:227], v[164:167], v[116:119]
	v_mfma_f32_16x16x32_bf16 v[108:111], v[232:235], v[164:167], v[108:111]
	ds_read_b128 v[164:167], v146 offset:16384
	v_mfma_f32_16x16x32_bf16 v[100:103], v[224:227], v[176:179], v[100:103]
	v_mfma_f32_16x16x32_bf16 v[92:95], v[232:235], v[176:179], v[92:95]
	ds_read_b128 v[176:179], v146 offset:18432
	v_mfma_f32_16x16x32_bf16 v[84:87], v[224:227], v[208:211], v[84:87]
	v_mfma_f32_16x16x32_bf16 v[76:79], v[232:235], v[208:211], v[76:79]
	ds_read_b128 v[208:211], v146 offset:20480
	v_mfma_f32_16x16x32_bf16 v[68:71], v[224:227], v[216:219], v[68:71]
	v_mfma_f32_16x16x32_bf16 v[64:67], v[232:235], v[216:219], v[64:67]
	ds_read_b128 v[216:219], v146 offset:22528
	v_mfma_f32_16x16x32_bf16 v[116:119], v[228:231], v[172:175], v[116:119]
	v_mfma_f32_16x16x32_bf16 v[108:111], v[236:239], v[172:175], v[108:111]
	ds_read_b128 v[172:175], v146 offset:17408
	v_mfma_f32_16x16x32_bf16 v[100:103], v[228:231], v[180:183], v[100:103]
	v_mfma_f32_16x16x32_bf16 v[92:95], v[236:239], v[180:183], v[92:95]
	ds_read_b128 v[180:183], v146 offset:19456
	v_mfma_f32_16x16x32_bf16 v[84:87], v[228:231], v[212:215], v[84:87]
	v_mfma_f32_16x16x32_bf16 v[76:79], v[236:239], v[212:215], v[76:79]
	ds_read_b128 v[212:215], v146 offset:21504
	v_mfma_f32_16x16x32_bf16 v[68:71], v[228:231], v[220:223], v[68:71]
	v_mfma_f32_16x16x32_bf16 v[64:67], v[236:239], v[220:223], v[64:67]
	ds_read_b128 v[220:223], v146 offset:23552
	s_barrier
	s_setprio 0
	s_mov_b32 m0, s43
	v_lshl_add_u64 v[188:189], s[28:29], 0, v[128:129]
	global_load_lds_dwordx4 v[188:189], off
	v_lshl_add_u64 v[240:241], s[28:29], 0, v[134:135]
	s_mov_b32 m0, s44
	s_nop 0
	global_load_lds_dwordx4 v[240:241], off
	s_waitcnt vmcnt(8)
	s_setprio 1
	s_barrier
	s_waitcnt lgkmcnt(0)
	v_mfma_f32_16x16x32_bf16 v[60:63], v[148:151], v[164:167], v[60:63]
	v_mfma_f32_16x16x32_bf16 v[56:59], v[156:159], v[164:167], v[56:59]
	v_mfma_f32_16x16x32_bf16 v[40:43], v[148:151], v[176:179], v[40:43]
	v_mfma_f32_16x16x32_bf16 v[32:35], v[156:159], v[176:179], v[32:35]
	v_mfma_f32_16x16x32_bf16 v[16:19], v[148:151], v[208:211], v[16:19]
	v_mfma_f32_16x16x32_bf16 v[12:15], v[156:159], v[208:211], v[12:15]
	v_mfma_f32_16x16x32_bf16 v[4:7], v[148:151], v[216:219], v[4:7]
	v_mfma_f32_16x16x32_bf16 v[0:3], v[156:159], v[216:219], v[0:3]
	v_mfma_f32_16x16x32_bf16 v[60:63], v[152:155], v[172:175], v[60:63]
	v_mfma_f32_16x16x32_bf16 v[56:59], v[160:163], v[172:175], v[56:59]
	v_mfma_f32_16x16x32_bf16 v[40:43], v[152:155], v[180:183], v[40:43]
	v_mfma_f32_16x16x32_bf16 v[32:35], v[160:163], v[180:183], v[32:35]
	v_mfma_f32_16x16x32_bf16 v[16:19], v[152:155], v[212:215], v[16:19]
	v_mfma_f32_16x16x32_bf16 v[12:15], v[160:163], v[212:215], v[12:15]
	v_mfma_f32_16x16x32_bf16 v[4:7], v[152:155], v[220:223], v[4:7]
	v_mfma_f32_16x16x32_bf16 v[0:3], v[160:163], v[220:223], v[0:3]
	s_barrier
	s_setprio 0
	s_add_u32 s58, s26, 0x2000
	s_addc_u32 s59, s27, 0
	s_add_i32 s57, s60, s42
	v_lshl_add_u64 v[148:149], s[58:59], 0, v[168:169]
	s_mov_b32 m0, s57
	s_nop 0
	global_load_lds_dwordx4 v[148:149], off
	v_lshl_add_u64 v[148:149], s[58:59], 0, v[132:133]
	s_add_i32 m0, s57, 0x2000
	s_nop 0
	global_load_lds_dwordx4 v[148:149], off
	s_waitcnt vmcnt(6)
	s_setprio 1
	s_barrier
	v_mfma_f32_16x16x32_bf16 v[44:47], v[224:227], v[164:167], v[44:47]
	v_mfma_f32_16x16x32_bf16 v[36:39], v[232:235], v[164:167], v[36:39]
	ds_read_b128 v[164:167], v146 offset:32768
	v_mfma_f32_16x16x32_bf16 v[20:23], v[224:227], v[176:179], v[20:23]
	v_mfma_f32_16x16x32_bf16 v[8:11], v[232:235], v[176:179], v[8:11]
	ds_read_b128 v[176:179], v146 offset:34816
	v_mfma_f32_16x16x32_bf16 v[52:55], v[224:227], v[208:211], v[52:55]
	v_mfma_f32_16x16x32_bf16 v[48:51], v[232:235], v[208:211], v[48:51]
	ds_read_b128 v[208:211], v146 offset:36864
	v_mfma_f32_16x16x32_bf16 v[28:31], v[224:227], v[216:219], v[28:31]
	v_mfma_f32_16x16x32_bf16 v[24:27], v[232:235], v[216:219], v[24:27]
	ds_read_b128 v[216:219], v146 offset:38912
	v_mfma_f32_16x16x32_bf16 v[44:47], v[228:231], v[172:175], v[44:47]
	v_mfma_f32_16x16x32_bf16 v[36:39], v[236:239], v[172:175], v[36:39]
	ds_read_b128 v[172:175], v146 offset:33792
	v_mfma_f32_16x16x32_bf16 v[20:23], v[228:231], v[180:183], v[20:23]
	v_mfma_f32_16x16x32_bf16 v[8:11], v[236:239], v[180:183], v[8:11]
	ds_read_b128 v[180:183], v146 offset:35840
	v_mfma_f32_16x16x32_bf16 v[52:55], v[228:231], v[212:215], v[52:55]
	v_mfma_f32_16x16x32_bf16 v[48:51], v[236:239], v[212:215], v[48:51]
	ds_read_b128 v[212:215], v146 offset:37888
	v_mfma_f32_16x16x32_bf16 v[28:31], v[228:231], v[220:223], v[28:31]
	v_mfma_f32_16x16x32_bf16 v[24:27], v[236:239], v[220:223], v[24:27]
	ds_read_b128 v[220:223], v146 offset:39936
	s_barrier
	s_setprio 0
	s_add_i32 s57, 0, 0x18000
	v_add_u32_e32 v147, s57, v145
	ds_read_b128 v[148:151], v147
	ds_read_b128 v[152:155], v147 offset:1024
	ds_read_b128 v[156:159], v147 offset:2048
	ds_read_b128 v[160:163], v147 offset:3072
	s_mov_b32 m0, s45
	v_lshl_add_u64 v[224:225], s[28:29], 0, v[130:131]
	global_load_lds_dwordx4 v[224:225], off
	v_lshl_add_u64 v[224:225], s[28:29], 0, v[136:137]
	s_mov_b32 m0, s46
	s_nop 0
	global_load_lds_dwordx4 v[224:225], off
	s_waitcnt lgkmcnt(0)
	s_setprio 1
	s_barrier
	s_waitcnt lgkmcnt(0)
	v_mfma_f32_16x16x32_bf16 v[124:127], v[148:151], v[164:167], v[124:127]
	v_mfma_f32_16x16x32_bf16 v[120:123], v[156:159], v[164:167], v[120:123]
	v_mfma_f32_16x16x32_bf16 v[112:115], v[148:151], v[176:179], v[112:115]
	v_mfma_f32_16x16x32_bf16 v[104:107], v[156:159], v[176:179], v[104:107]
	v_mfma_f32_16x16x32_bf16 v[96:99], v[148:151], v[208:211], v[96:99]
	v_mfma_f32_16x16x32_bf16 v[88:91], v[156:159], v[208:211], v[88:91]
	v_mfma_f32_16x16x32_bf16 v[80:83], v[148:151], v[216:219], v[80:83]
	v_mfma_f32_16x16x32_bf16 v[72:75], v[156:159], v[216:219], v[72:75]
	v_mfma_f32_16x16x32_bf16 v[124:127], v[152:155], v[172:175], v[124:127]
	v_mfma_f32_16x16x32_bf16 v[120:123], v[160:163], v[172:175], v[120:123]
	v_mfma_f32_16x16x32_bf16 v[112:115], v[152:155], v[180:183], v[112:115]
	v_mfma_f32_16x16x32_bf16 v[104:107], v[160:163], v[180:183], v[104:107]
	v_mfma_f32_16x16x32_bf16 v[96:99], v[152:155], v[212:215], v[96:99]
	v_mfma_f32_16x16x32_bf16 v[88:91], v[160:163], v[212:215], v[88:91]
	v_mfma_f32_16x16x32_bf16 v[80:83], v[152:155], v[220:223], v[80:83]
	v_mfma_f32_16x16x32_bf16 v[72:75], v[160:163], v[220:223], v[72:75]
	s_barrier
	s_setprio 0
	s_add_i32 s28, 0, 0x1c000
	s_add_i32 s29, s57, s42
	v_add_u32_e32 v147, s28, v145
	v_lshl_add_u64 v[170:171], v[170:171], 0, s[94:95]
	s_mov_b32 m0, s29
	ds_read_b128 v[224:227], v147
	ds_read_b128 v[228:231], v147 offset:1024
	ds_read_b128 v[232:235], v147 offset:2048
	ds_read_b128 v[236:239], v147 offset:3072
	global_load_lds_dwordx4 v[170:171], off
	v_lshl_add_u64 v[170:171], v[184:185], 0, s[94:95]
	s_add_i32 m0, s29, 0x2000
	s_nop 0
	global_load_lds_dwordx4 v[170:171], off
	s_setprio 1
	s_barrier
	s_waitcnt lgkmcnt(0)
	v_mfma_f32_16x16x32_bf16 v[116:119], v[224:227], v[164:167], v[116:119]
	v_mfma_f32_16x16x32_bf16 v[108:111], v[232:235], v[164:167], v[108:111]
	ds_read_b128 v[164:167], v146 offset:49152
	v_mfma_f32_16x16x32_bf16 v[100:103], v[224:227], v[176:179], v[100:103]
	v_mfma_f32_16x16x32_bf16 v[92:95], v[232:235], v[176:179], v[92:95]
	ds_read_b128 v[176:179], v146 offset:51200
	v_mfma_f32_16x16x32_bf16 v[84:87], v[224:227], v[208:211], v[84:87]
	v_mfma_f32_16x16x32_bf16 v[76:79], v[232:235], v[208:211], v[76:79]
	ds_read_b128 v[208:211], v146 offset:53248
	v_mfma_f32_16x16x32_bf16 v[68:71], v[224:227], v[216:219], v[68:71]
	v_mfma_f32_16x16x32_bf16 v[64:67], v[232:235], v[216:219], v[64:67]
	ds_read_b128 v[216:219], v146 offset:55296
	v_mfma_f32_16x16x32_bf16 v[116:119], v[228:231], v[172:175], v[116:119]
	v_mfma_f32_16x16x32_bf16 v[108:111], v[236:239], v[172:175], v[108:111]
	ds_read_b128 v[172:175], v146 offset:50176
	v_mfma_f32_16x16x32_bf16 v[100:103], v[228:231], v[180:183], v[100:103]
	v_mfma_f32_16x16x32_bf16 v[92:95], v[236:239], v[180:183], v[92:95]
	ds_read_b128 v[180:183], v146 offset:52224
	v_mfma_f32_16x16x32_bf16 v[84:87], v[228:231], v[212:215], v[84:87]
	v_mfma_f32_16x16x32_bf16 v[76:79], v[236:239], v[212:215], v[76:79]
	ds_read_b128 v[212:215], v146 offset:54272
	v_mfma_f32_16x16x32_bf16 v[68:71], v[228:231], v[220:223], v[68:71]
	v_mfma_f32_16x16x32_bf16 v[64:67], v[236:239], v[220:223], v[64:67]
	ds_read_b128 v[220:223], v146 offset:56320
	s_barrier
	s_setprio 0
	s_mov_b32 m0, s47
	v_lshl_add_u64 v[170:171], v[188:189], 0, s[94:95]
	global_load_lds_dwordx4 v[170:171], off
	v_lshl_add_u64 v[170:171], v[240:241], 0, s[94:95]
	s_mov_b32 m0, s48
	s_nop 0
	global_load_lds_dwordx4 v[170:171], off
	s_waitcnt vmcnt(8)
	s_setprio 1
	s_barrier
	s_waitcnt lgkmcnt(0)
	v_mfma_f32_16x16x32_bf16 v[60:63], v[148:151], v[164:167], v[60:63]
	v_mfma_f32_16x16x32_bf16 v[56:59], v[156:159], v[164:167], v[56:59]
	v_mfma_f32_16x16x32_bf16 v[40:43], v[148:151], v[176:179], v[40:43]
	v_mfma_f32_16x16x32_bf16 v[32:35], v[156:159], v[176:179], v[32:35]
	v_mfma_f32_16x16x32_bf16 v[16:19], v[148:151], v[208:211], v[16:19]
	v_mfma_f32_16x16x32_bf16 v[12:15], v[156:159], v[208:211], v[12:15]
	v_mfma_f32_16x16x32_bf16 v[4:7], v[148:151], v[216:219], v[4:7]
	v_mfma_f32_16x16x32_bf16 v[0:3], v[156:159], v[216:219], v[0:3]
	v_mfma_f32_16x16x32_bf16 v[60:63], v[152:155], v[172:175], v[60:63]
	v_mfma_f32_16x16x32_bf16 v[56:59], v[160:163], v[172:175], v[56:59]
	v_mfma_f32_16x16x32_bf16 v[40:43], v[152:155], v[180:183], v[40:43]
	v_mfma_f32_16x16x32_bf16 v[32:35], v[160:163], v[180:183], v[32:35]
	v_mfma_f32_16x16x32_bf16 v[16:19], v[152:155], v[212:215], v[16:19]
	v_mfma_f32_16x16x32_bf16 v[12:15], v[160:163], v[212:215], v[12:15]
	v_mfma_f32_16x16x32_bf16 v[4:7], v[152:155], v[220:223], v[4:7]
	v_mfma_f32_16x16x32_bf16 v[0:3], v[160:163], v[220:223], v[0:3]
	s_barrier
	s_setprio 0
	s_add_u32 s26, s26, 0x2080
	s_addc_u32 s27, s27, 0
	s_add_i32 s28, s28, s42
	v_lshl_add_u64 v[148:149], s[26:27], 0, v[168:169]
	s_mov_b32 m0, s28
	s_nop 0
	global_load_lds_dwordx4 v[148:149], off
	v_lshl_add_u64 v[148:149], s[26:27], 0, v[132:133]
	s_add_i32 m0, s28, 0x2000
	s_nop 0
	global_load_lds_dwordx4 v[148:149], off
	s_waitcnt vmcnt(6)
	s_setprio 1
	s_barrier
	v_mfma_f32_16x16x32_bf16 v[44:47], v[224:227], v[164:167], v[44:47]
	v_mfma_f32_16x16x32_bf16 v[36:39], v[232:235], v[164:167], v[36:39]
	ds_read_b128 v[164:167], v146
	v_mfma_f32_16x16x32_bf16 v[20:23], v[224:227], v[176:179], v[20:23]
	v_mfma_f32_16x16x32_bf16 v[8:11], v[232:235], v[176:179], v[8:11]
	ds_read_b128 v[176:179], v146 offset:2048
	v_mfma_f32_16x16x32_bf16 v[52:55], v[224:227], v[208:211], v[52:55]
	v_mfma_f32_16x16x32_bf16 v[48:51], v[232:235], v[208:211], v[48:51]
	ds_read_b128 v[208:211], v146 offset:4096
	v_mfma_f32_16x16x32_bf16 v[28:31], v[224:227], v[216:219], v[28:31]
	v_mfma_f32_16x16x32_bf16 v[24:27], v[232:235], v[216:219], v[24:27]
	ds_read_b128 v[216:219], v146 offset:6144
	v_mfma_f32_16x16x32_bf16 v[44:47], v[228:231], v[172:175], v[44:47]
	v_mfma_f32_16x16x32_bf16 v[36:39], v[236:239], v[172:175], v[36:39]
	ds_read_b128 v[172:175], v146 offset:1024
	v_mfma_f32_16x16x32_bf16 v[20:23], v[228:231], v[180:183], v[20:23]
	v_mfma_f32_16x16x32_bf16 v[8:11], v[236:239], v[180:183], v[8:11]
	ds_read_b128 v[180:183], v146 offset:3072
	v_mfma_f32_16x16x32_bf16 v[52:55], v[228:231], v[212:215], v[52:55]
	v_mfma_f32_16x16x32_bf16 v[48:51], v[236:239], v[212:215], v[48:51]
	ds_read_b128 v[212:215], v146 offset:5120
	v_mfma_f32_16x16x32_bf16 v[28:31], v[228:231], v[220:223], v[28:31]
	v_mfma_f32_16x16x32_bf16 v[24:27], v[236:239], v[220:223], v[24:27]
	ds_read_b128 v[220:223], v146 offset:7168
	s_barrier
	s_setprio 0
	s_add_i32 s56, s56, 2
	s_add_u32 s24, s24, 0x100
	s_addc_u32 s25, s25, 0
	s_add_u32 s34, s34, 0x100
	s_addc_u32 s35, s35, 0
	s_cmp_gt_u32 s56, 5
	s_cbranch_scc0 .LBB0_1521
	s_waitcnt lgkmcnt(0)
	s_and_b64 vcc, exec, s[6:7]
	s_cbranch_vccz .LBB0_1524
	s_barrier
